# mLSTM phase C head-norm: ds_bpermute butterflies -> DPP adds, precise 1/sqrt -> v_rsq (hazard distances kept)
# speedup vs baseline: 1.0206x; 1.0020x over previous
; __device__ __forceinline__ float fast_sigmoid(float x) { return __builtin_amdgcn_rcpf(1.0f + __expf(-x)); }
; #define LAS __attribute__((address_space(3)))
; __device__ __forceinline__ unsigned pk2(float lo, float hi) { return pg8::cvt_pk_bf16(lo, hi); }
; #define WG_BAR() do { asm volatile("s_waitcnt lgkmcnt(0)" ::: "memory"); __builtin_amdgcn_s_barrier(); asm volatile("" ::: "memory"); } while (0)
; template <class AT_>
; __device__ __forceinline__ void mlstm_phase_c(const AT_& a, Frame& F, int j) {
;     ...
;         const float inv = 1.0f / fmaxf(fabsf(den), __expf(-mout));
;         WG_BAR();
;         if (has) MLC_LOAD_C(nit);
; #pragma unroll
;         for (int db = 0; db < 2; ++db)
; #pragma unroll
;             for (int g4 = 0; g4 < 4; ++g4) { f32x4 o; o.x = accn[db][4 * g4] * inv; o.y = accn[db][4 * g4 + 1] * inv; o.z = accn[db][4 * g4 + 2] * inv; o.w = accn[db][4 * g4 + 3] * inv;
;                 *(LAS f32x4*)(hbuf + t * 260 + 64 * dq + 32 * db + 8 * g4 + 4 * hh) = o; }
;         WG_BAR();
;         const f32x4 gn = *(const f32x4*)(hgain + h * ML_DV + 4 * lane);
; #pragma unroll
;         for (int i = 0; i < 8; ++i) { const int tt = 8 * w + i; const f32x4 v = *(const LAS f32x4*)(hbuf + tt * 260 + 4 * lane);
;             const float ss = wave_sum((v.x * v.x + v.y * v.y) + (v.z * v.z + v.w * v.w)); const float rstd = 1.0f / sqrtf(ss * (1.0f / ML_DV) + NORM_EPS);
;             const v2u ow = ogw[i];
;             f32x4 y = v * rstd * gn; y.x *= pg8::fast_sigmoid(bflo(ow.x)); y.y *= pg8::fast_sigmoid(bfhi(ow.x)); y.z *= pg8::fast_sigmoid(bflo(ow.y)); y.w *= pg8::fast_sigmoid(bfhi(ow.y));
;             v2u o; o.x = pk2(y.x, y.y); o.y = pk2(y.z, y.w);
;             *(v2u*)(HS + (size_t)(tok0 + tt) * DM + h * 256 + 4 * lane) = o; }
.LBB0_644:
	s_or_b64 exec, exec, s[74:75]
	v_mul_f32_e32 v2, 0xbfb8aa3b, v237
	v_exp_f32_e32 v2, v2
	v_add_f32_e32 v6, v238, v239
	s_waitcnt lgkmcnt(0)
	v_add_f32_e32 v4, v4, v5
	v_fmac_f32_e32 v6, v166, v4
	v_max_f32_e64 v2, |v6|, v2
	v_div_scale_f32 v4, s[2:3], v2, v2, 1.0
	v_rcp_f32_e32 v5, v4
	v_div_scale_f32 v6, vcc, 1.0, v2, 1.0
	v_and_b32_e32 v26, 0x700, v205
	v_fma_f32 v7, -v4, v5, 1.0
	v_fmac_f32_e32 v5, v7, v5
	v_mul_f32_e32 v7, v6, v5
	v_fma_f32 v8, -v4, v7, v6
	v_fmac_f32_e32 v7, v8, v5
	v_fma_f32 v4, -v4, v7, v6
	v_div_fmas_f32 v4, v4, v5, v7
	v_div_fixup_f32 v2, v4, v2, 1.0
	v_pk_mul_f32 v[4:5], v[36:37], v[2:3] op_sel_hi:[1,0]
	v_pk_mul_f32 v[6:7], v[38:39], v[2:3] op_sel_hi:[1,0]
	ds_write_b128 v227, v[4:7] offset:1024
	v_pk_mul_f32 v[4:5], v[40:41], v[2:3] op_sel_hi:[1,0]
	v_pk_mul_f32 v[6:7], v[42:43], v[2:3] op_sel_hi:[1,0]
	ds_write_b128 v227, v[4:7] offset:1056
	v_pk_mul_f32 v[4:5], v[44:45], v[2:3] op_sel_hi:[1,0]
	v_pk_mul_f32 v[6:7], v[46:47], v[2:3] op_sel_hi:[1,0]
	ds_write_b128 v227, v[4:7] offset:1088
	v_pk_mul_f32 v[4:5], v[48:49], v[2:3] op_sel_hi:[1,0]
	v_pk_mul_f32 v[6:7], v[50:51], v[2:3] op_sel_hi:[1,0]
	ds_write_b128 v227, v[4:7] offset:1120
	v_pk_mul_f32 v[4:5], v[52:53], v[2:3] op_sel_hi:[1,0]
	v_pk_mul_f32 v[6:7], v[54:55], v[2:3] op_sel_hi:[1,0]
	ds_write_b128 v227, v[4:7] offset:1152
	v_pk_mul_f32 v[4:5], v[56:57], v[2:3] op_sel_hi:[1,0]
	v_pk_mul_f32 v[6:7], v[58:59], v[2:3] op_sel_hi:[1,0]
	ds_write_b128 v227, v[4:7] offset:1184
	v_pk_mul_f32 v[4:5], v[60:61], v[2:3] op_sel_hi:[1,0]
	v_pk_mul_f32 v[6:7], v[62:63], v[2:3] op_sel_hi:[1,0]
	ds_write_b128 v227, v[4:7] offset:1216
	v_pk_mul_f32 v[4:5], v[64:65], v[2:3] op_sel_hi:[1,0]
	v_pk_mul_f32 v[6:7], v[66:67], v[2:3] op_sel_hi:[1,0]
	ds_write_b128 v227, v[4:7] offset:1248
	s_waitcnt lgkmcnt(0)
	s_barrier
	v_add_u32_e32 v8, s8, v215
	ds_read_b128 v[22:25], v8 offset:1024
	v_lshlrev_b32_e32 v2, 2, v26
	v_lshl_add_u64 v[4:5], v[188:189], 0, v[2:3]
	v_xor_b32_e32 v2, 1, v226
	v_cmp_lt_i32_e32 vcc, v2, v236
	s_waitcnt lgkmcnt(0)
	v_pk_mul_f32 v[12:13], v[24:25], v[24:25]
	v_pk_mul_f32 v[18:19], v[22:23], v[22:23]
	global_load_dwordx4 v[4:7], v[4:5], off
	v_pk_mov_b32 v[20:21], v[18:19], v[12:13] op_sel:[1,0]
	v_mov_b32_e32 v19, v13
	v_cndmask_b32_e32 v2, v226, v2, vcc
	v_pk_add_f32 v[12:13], v[20:21], v[18:19]
	v_lshlrev_b32_e32 v14, 2, v2
	v_add_f32_e32 v2, v12, v13
	s_nop 0
	v_xor_b32_e32 v13, 2, v226
	v_cmp_lt_i32_e32 vcc, v13, v236
	s_mul_i32 s2, s9, 0x410
	v_add_u32_e32 v16, s2, v215
	v_cndmask_b32_e32 v13, v226, v13, vcc
	v_lshlrev_b32_e32 v17, 2, v13
	s_waitcnt lgkmcnt(0)
	s_nop 1
	v_add_f32_dpp v2, v2, v2 quad_perm:[1,0,3,2] row_mask:0xf bank_mask:0xf bound_ctrl:1
	s_nop 0
	v_xor_b32_e32 v13, 4, v226
	v_cmp_lt_i32_e32 vcc, v13, v236
	ds_read_b128 v[8:11], v16 offset:1024
	s_waitcnt lgkmcnt(0)
	s_nop 1
	v_add_f32_dpp v2, v2, v2 quad_perm:[2,3,0,1] row_mask:0xf bank_mask:0xf bound_ctrl:1
	v_cndmask_b32_e32 v13, v226, v13, vcc
	v_lshlrev_b32_e32 v18, 2, v13
	s_nop 0
	v_xor_b32_e32 v13, 8, v226
	v_cmp_lt_i32_e32 vcc, v13, v236
	s_waitcnt lgkmcnt(0)
	s_nop 1
	v_add_f32_dpp v2, v2, v2 row_half_mirror row_mask:0xf bank_mask:0xf bound_ctrl:1
	v_cndmask_b32_e32 v13, v226, v13, vcc
	v_lshlrev_b32_e32 v19, 2, v13
	s_nop 0
	v_xor_b32_e32 v13, 16, v226
	v_cmp_lt_i32_e32 vcc, v13, v236
	s_waitcnt lgkmcnt(0)
	s_nop 1
	v_add_f32_dpp v2, v2, v2 row_mirror row_mask:0xf bank_mask:0xf bound_ctrl:1
	v_cndmask_b32_e32 v13, v226, v13, vcc
	v_lshlrev_b32_e32 v20, 2, v13
	s_nop 0
	v_and_b32_e32 v13, 0xfc0, v209
	s_waitcnt lgkmcnt(0)
	s_nop 1
	v_add_f32_dpp v2, v2, v2 row_bcast:15 row_mask:0xa bank_mask:0xf
	s_nop 0
	s_waitcnt lgkmcnt(0)
	s_nop 1
	v_add_f32_dpp v2, v2, v2 row_bcast:31 row_mask:0xc bank_mask:0xf
	s_nop 0
	v_readlane_b32 s98, v2, 63
	s_nop 1
	v_mov_b32_e32 v2, s98
	v_fmamk_f32 v2, v2, 0x3b800000, v228
	v_rsq_f32_e32 v244, v2
	s_nop 1
	s_nop 1
	s_nop 1
	s_nop 0
	s_nop 1
	s_nop 0
	s_nop 1
	s_nop 1
	s_nop 1
	s_nop 1
	s_nop 1
	s_movk_i32 s2, 0xf000
	v_lshlrev_b32_e32 v2, 1, v26
	v_and_or_b32 v15, v207, s2, v13
	v_lshl_add_u64 v[12:13], v[194:195], 0, v[2:3]
	s_nop 1
	v_pk_mul_f32 v[26:27], v[10:11], v[10:11]
	v_pk_mul_f32 v[28:29], v[8:9], v[8:9]
	v_mov_b32_e32 v2, v244
	v_pk_mov_b32 v[30:31], v[28:29], v[26:27] op_sel:[1,0]
	v_mov_b32_e32 v29, v27
	v_pk_add_f32 v[26:27], v[30:31], v[28:29]
	v_pk_mul_f32 v[22:23], v[22:23], v[2:3] op_sel_hi:[1,0]
	v_add_f32_e32 v21, v26, v27
	s_nop 0
	v_pk_mul_f32 v[24:25], v[24:25], v[2:3] op_sel_hi:[1,0]
	v_lshlrev_b32_e32 v2, 16, v168
	v_mul_f32_e32 v2, 0xbfb8aa3b, v2
	v_exp_f32_e32 v2, v2
	s_waitcnt lgkmcnt(0)
	s_nop 1
	v_add_f32_dpp v21, v21, v21 quad_perm:[1,0,3,2] row_mask:0xf bank_mask:0xf bound_ctrl:1
	s_nop 0
	s_waitcnt vmcnt(0)
	v_pk_mul_f32 v[22:23], v[4:5], v[22:23]
	v_add_f32_e32 v2, 1.0, v2
	v_rcp_f32_e32 v2, v2
	v_and_b32_e32 v27, 0xffff0000, v168
	s_waitcnt lgkmcnt(0)
	s_nop 1
	v_add_f32_dpp v21, v21, v21 quad_perm:[2,3,0,1] row_mask:0xf bank_mask:0xf bound_ctrl:1
	v_mul_f32_e32 v27, 0xbfb8aa3b, v27
	v_mul_f32_e32 v2, v2, v22
	s_nop 0
	v_exp_f32_e32 v27, v27
	v_and_b32_e32 v28, 0xffff0000, v169
	v_mul_f32_e32 v28, 0xbfb8aa3b, v28
	v_pk_mul_f32 v[24:25], v[6:7], v[24:25]
	s_waitcnt lgkmcnt(0)
	s_nop 1
	v_add_f32_dpp v21, v21, v21 row_half_mirror row_mask:0xf bank_mask:0xf bound_ctrl:1
	s_nop 0
	v_add_f32_e32 v26, 1.0, v27
	v_rcp_f32_e32 v26, v26
	v_lshlrev_b32_e32 v27, 16, v169
	v_mul_f32_e32 v27, 0xbfb8aa3b, v27
	s_waitcnt lgkmcnt(0)
	s_nop 1
	v_add_f32_dpp v21, v21, v21 row_mirror row_mask:0xf bank_mask:0xf bound_ctrl:1
	s_nop 0
	v_exp_f32_e32 v27, v27
	v_exp_f32_e32 v28, v28
	s_waitcnt lgkmcnt(0)
; __device__ __forceinline__ float fast_sigmoid(float x) { return __builtin_amdgcn_rcpf(1.0f + __expf(-x)); }
; #define LAS __attribute__((address_space(3)))
; __device__ __forceinline__ unsigned pk2(float lo, float hi) { return pg8::cvt_pk_bf16(lo, hi); }
; template <class AT_>
; __device__ __forceinline__ void mlstm_phase_c(const AT_& a, Frame& F, int j) {
;     ...
; #pragma unroll
;         for (int i = 0; i < 8; ++i) { const int tt = 8 * w + i; const f32x4 v = *(const LAS f32x4*)(hbuf + tt * 260 + 4 * lane);
;             const float ss = wave_sum((v.x * v.x + v.y * v.y) + (v.z * v.z + v.w * v.w)); const float rstd = 1.0f / sqrtf(ss * (1.0f / ML_DV) + NORM_EPS);
;             const v2u ow = ogw[i];
;             f32x4 y = v * rstd * gn; y.x *= pg8::fast_sigmoid(bflo(ow.x)); y.y *= pg8::fast_sigmoid(bfhi(ow.x)); y.z *= pg8::fast_sigmoid(bflo(ow.y)); y.w *= pg8::fast_sigmoid(bfhi(ow.y));
;             v2u o; o.x = pk2(y.x, y.y); o.y = pk2(y.z, y.w);
;             *(v2u*)(HS + (size_t)(tok0 + tt) * DM + h * 256 + 4 * lane) = o; }
	s_nop 1
	v_add_f32_dpp v21, v21, v21 row_bcast:15 row_mask:0xa bank_mask:0xf
	s_nop 0
	v_mul_f32_e32 v22, v26, v23
	v_cvt_pk_bf16_f32 v22, v2, v22
	v_add_f32_e32 v27, 1.0, v27
	v_rcp_f32_e32 v27, v27
	s_waitcnt lgkmcnt(0)
	s_nop 1
	v_add_f32_dpp v2, v21, v21 row_bcast:31 row_mask:0xc bank_mask:0xf
	s_nop 0
	v_readlane_b32 s98, v2, 63
	s_nop 1
	v_mov_b32_e32 v2, s98
	v_fmamk_f32 v2, v2, 0x3b800000, v228
	v_rsq_f32_e32 v245, v2
	s_nop 1
	v_mul_f32_e32 v23, v27, v24
	v_add_f32_e32 v28, 1.0, v28
	s_nop 1
	v_rcp_f32_e32 v28, v28
	s_nop 1
	v_mul_f32_e32 v24, v28, v25
	s_nop 1
	v_cvt_pk_bf16_f32 v23, v23, v24
	v_add_u32_e32 v24, s84, v15
	s_nop 1
	v_ashrrev_i32_e32 v25, 31, v24
	v_lshlrev_b64 v[24:25], 12, v[24:25]
	s_nop 1
	v_lshl_add_u64 v[24:25], v[12:13], 0, v[24:25]
	global_store_dwordx2 v[24:25], v[22:23], off
	s_nop 1
	v_mov_b32_e32 v2, v245
	v_pk_mul_f32 v[26:27], v[8:9], v[2:3] op_sel_hi:[1,0]
	v_pk_mul_f32 v[28:29], v[10:11], v[2:3] op_sel_hi:[1,0]
	ds_read_b128 v[8:11], v16 offset:2064
	ds_read_b128 v[22:25], v16 offset:3104
	v_lshlrev_b32_e32 v2, 16, v170
	v_mul_f32_e32 v2, 0xbfb8aa3b, v2
	v_exp_f32_e32 v2, v2
	s_waitcnt lgkmcnt(0)
	v_pk_mul_f32 v[30:31], v[10:11], v[10:11]
	v_pk_mul_f32 v[32:33], v[8:9], v[8:9]
	v_pk_mul_f32 v[26:27], v[4:5], v[26:27]
	v_pk_mov_b32 v[34:35], v[32:33], v[30:31] op_sel:[1,0]
	v_mov_b32_e32 v33, v31
	v_pk_add_f32 v[30:31], v[34:35], v[32:33]
	v_add_f32_e32 v2, 1.0, v2
	v_add_f32_e32 v21, v30, v31
	s_nop 0
	v_rcp_f32_e32 v2, v2
	v_and_b32_e32 v31, 0xffff0000, v170
	v_mul_f32_e32 v31, 0xbfb8aa3b, v31
	v_exp_f32_e32 v31, v31
	s_waitcnt lgkmcnt(0)
	s_nop 1
	v_add_f32_dpp v21, v21, v21 quad_perm:[1,0,3,2] row_mask:0xf bank_mask:0xf bound_ctrl:1
	s_nop 0
	v_mul_f32_e32 v2, v2, v26
	v_and_b32_e32 v32, 0xffff0000, v171
	v_mul_f32_e32 v32, 0xbfb8aa3b, v32
	v_pk_mul_f32 v[28:29], v[6:7], v[28:29]
	s_waitcnt lgkmcnt(0)
	s_nop 1
	v_add_f32_dpp v21, v21, v21 quad_perm:[2,3,0,1] row_mask:0xf bank_mask:0xf bound_ctrl:1
	s_nop 0
	v_add_f32_e32 v30, 1.0, v31
	v_rcp_f32_e32 v30, v30
	v_lshlrev_b32_e32 v31, 16, v171
	v_mul_f32_e32 v31, 0xbfb8aa3b, v31
	s_waitcnt lgkmcnt(0)
	s_nop 1
	v_add_f32_dpp v21, v21, v21 row_half_mirror row_mask:0xf bank_mask:0xf bound_ctrl:1
	s_nop 0
	v_exp_f32_e32 v31, v31
	v_exp_f32_e32 v32, v32
	s_waitcnt lgkmcnt(0)
	s_nop 1
	v_add_f32_dpp v21, v21, v21 row_mirror row_mask:0xf bank_mask:0xf bound_ctrl:1
	s_nop 0
	v_add_f32_e32 v31, 1.0, v31
	v_rcp_f32_e32 v31, v31
	v_add_f32_e32 v32, 1.0, v32
	v_rcp_f32_e32 v32, v32
	s_waitcnt lgkmcnt(0)
	s_nop 1
	v_add_f32_dpp v21, v21, v21 row_bcast:15 row_mask:0xa bank_mask:0xf
	s_nop 0
	v_mul_f32_e32 v26, v30, v27
	v_cvt_pk_bf16_f32 v26, v2, v26
	v_mul_f32_e32 v27, v31, v28
	v_mul_f32_e32 v28, v32, v29
	s_waitcnt lgkmcnt(0)
	s_nop 1
	v_add_f32_dpp v2, v21, v21 row_bcast:31 row_mask:0xc bank_mask:0xf
	s_nop 0
	v_readlane_b32 s98, v2, 63
	s_nop 1
	v_mov_b32_e32 v2, s98
	v_fmamk_f32 v2, v2, 0x3b800000, v228
	v_rsq_f32_e32 v244, v2
	s_nop 1
	v_cvt_pk_bf16_f32 v27, v27, v28
	v_add_u32_e32 v28, s9, v15
	s_nop 1
	v_ashrrev_i32_e32 v29, 31, v28
	v_lshlrev_b64 v[28:29], 12, v[28:29]
	v_lshl_add_u64 v[28:29], v[12:13], 0, v[28:29]
	s_nop 1
	global_store_dwordx2 v[28:29], v[26:27], off
	s_nop 1
	s_nop 1
	s_nop 1
	s_nop 1
	s_nop 1
	s_nop 0
	s_nop 1
	v_pk_mul_f32 v[26:27], v[24:25], v[24:25]
	v_pk_mul_f32 v[28:29], v[22:23], v[22:23]
	v_mov_b32_e32 v2, v244
	v_pk_mov_b32 v[30:31], v[28:29], v[26:27] op_sel:[1,0]
	v_mov_b32_e32 v29, v27
	v_pk_add_f32 v[26:27], v[30:31], v[28:29]
	v_pk_mul_f32 v[8:9], v[8:9], v[2:3] op_sel_hi:[1,0]
	v_add_f32_e32 v21, v26, v27
	v_pk_mul_f32 v[10:11], v[10:11], v[2:3] op_sel_hi:[1,0]
	v_lshlrev_b32_e32 v2, 16, v172
	s_nop 0
	v_mul_f32_e32 v2, 0xbfb8aa3b, v2
	v_exp_f32_e32 v2, v2
	v_pk_mul_f32 v[8:9], v[4:5], v[8:9]
	v_and_b32_e32 v27, 0xffff0000, v172
	s_waitcnt lgkmcnt(0)
	s_nop 1
	v_add_f32_dpp v21, v21, v21 quad_perm:[1,0,3,2] row_mask:0xf bank_mask:0xf bound_ctrl:1
	v_add_f32_e32 v2, 1.0, v2
	s_nop 0
	v_rcp_f32_e32 v2, v2
	v_mul_f32_e32 v27, 0xbfb8aa3b, v27
	v_exp_f32_e32 v27, v27
	v_and_b32_e32 v28, 0xffff0000, v173
	v_mul_f32_e32 v2, v2, v8
	s_waitcnt lgkmcnt(0)
	s_nop 1
	v_add_f32_dpp v8, v21, v21 quad_perm:[2,3,0,1] row_mask:0xf bank_mask:0xf bound_ctrl:1
	s_nop 0
	v_add_f32_e32 v26, 1.0, v27
	v_lshlrev_b32_e32 v27, 16, v173
	v_mul_f32_e32 v27, 0xbfb8aa3b, v27
	v_mul_f32_e32 v28, 0xbfb8aa3b, v28
	s_waitcnt lgkmcnt(0)
	s_nop 1
	v_add_f32_dpp v8, v8, v8 row_half_mirror row_mask:0xf bank_mask:0xf bound_ctrl:1
	s_nop 0
	v_exp_f32_e32 v27, v27
	v_exp_f32_e32 v28, v28
	v_rcp_f32_e32 v26, v26
	v_pk_mul_f32 v[10:11], v[6:7], v[10:11]
	s_waitcnt lgkmcnt(0)
	s_nop 1
	v_add_f32_dpp v8, v8, v8 row_mirror row_mask:0xf bank_mask:0xf bound_ctrl:1
	s_nop 0
	v_add_f32_e32 v27, 1.0, v27
	v_add_f32_e32 v28, 1.0, v28
	v_rcp_f32_e32 v27, v27
	v_rcp_f32_e32 v28, v28
	s_waitcnt lgkmcnt(0)
	s_nop 1
	v_add_f32_dpp v21, v8, v8 row_bcast:15 row_mask:0xa bank_mask:0xf
	s_nop 0
	v_mul_f32_e32 v8, v26, v9
	v_cvt_pk_bf16_f32 v8, v2, v8
	v_mul_f32_e32 v9, v27, v10
	v_mul_f32_e32 v10, v28, v11
	s_waitcnt lgkmcnt(0)
	s_nop 1
	v_add_f32_dpp v2, v21, v21 row_bcast:31 row_mask:0xc bank_mask:0xf
	s_nop 0
	v_readlane_b32 s98, v2, 63
	s_nop 1
	v_mov_b32_e32 v2, s98
	v_fmamk_f32 v2, v2, 0x3b800000, v228
	v_rsq_f32_e32 v245, v2
	s_nop 1
	v_cvt_pk_bf16_f32 v9, v9, v10
	v_add_u32_e32 v10, s90, v15
	s_nop 1
	v_ashrrev_i32_e32 v11, 31, v10
	v_lshlrev_b64 v[10:11], 12, v[10:11]
	v_lshl_add_u64 v[10:11], v[12:13], 0, v[10:11]
	s_nop 1
	global_store_dwordx2 v[10:11], v[8:9], off
	s_nop 1
	s_nop 1
	s_nop 1
	s_nop 1
	s_nop 1
	s_nop 0
	s_nop 1
	v_mov_b32_e32 v2, v245
	ds_read_b128 v[8:11], v16 offset:4144
	v_pk_mul_f32 v[26:27], v[22:23], v[2:3] op_sel_hi:[1,0]
	v_pk_mul_f32 v[28:29], v[24:25], v[2:3] op_sel_hi:[1,0]
	ds_read_b128 v[22:25], v16 offset:5184
	v_lshlrev_b32_e32 v2, 16, v174
	s_waitcnt lgkmcnt(0)
; __device__ __forceinline__ float fast_sigmoid(float x) { return __builtin_amdgcn_rcpf(1.0f + __expf(-x)); }
; #define LAS __attribute__((address_space(3)))
; __device__ __forceinline__ unsigned pk2(float lo, float hi) { return pg8::cvt_pk_bf16(lo, hi); }
; template <class AT_>
; __device__ __forceinline__ void mlstm_phase_c(const AT_& a, Frame& F, int j) {
;     ...
; #pragma unroll
;         for (int i = 0; i < 8; ++i) { const int tt = 8 * w + i; const f32x4 v = *(const LAS f32x4*)(hbuf + tt * 260 + 4 * lane);
;             const float ss = wave_sum((v.x * v.x + v.y * v.y) + (v.z * v.z + v.w * v.w)); const float rstd = 1.0f / sqrtf(ss * (1.0f / ML_DV) + NORM_EPS);
;             const v2u ow = ogw[i];
;             f32x4 y = v * rstd * gn; y.x *= pg8::fast_sigmoid(bflo(ow.x)); y.y *= pg8::fast_sigmoid(bfhi(ow.x)); y.z *= pg8::fast_sigmoid(bflo(ow.y)); y.w *= pg8::fast_sigmoid(bfhi(ow.y));
;             v2u o; o.x = pk2(y.x, y.y); o.y = pk2(y.z, y.w);
;             *(v2u*)(HS + (size_t)(tok0 + tt) * DM + h * 256 + 4 * lane) = o; }
	v_pk_mul_f32 v[30:31], v[10:11], v[10:11]
	v_pk_mul_f32 v[32:33], v[8:9], v[8:9]
	v_mul_f32_e32 v2, 0xbfb8aa3b, v2
	v_pk_mov_b32 v[34:35], v[32:33], v[30:31] op_sel:[1,0]
	v_mov_b32_e32 v33, v31
	v_pk_add_f32 v[30:31], v[34:35], v[32:33]
	v_exp_f32_e32 v2, v2
	v_add_f32_e32 v21, v30, v31
	s_nop 0
	v_pk_mul_f32 v[26:27], v[4:5], v[26:27]
	v_add_f32_e32 v2, 1.0, v2
	v_rcp_f32_e32 v2, v2
	v_and_b32_e32 v31, 0xffff0000, v174
	s_waitcnt lgkmcnt(0)
	s_nop 1
	v_add_f32_dpp v21, v21, v21 quad_perm:[1,0,3,2] row_mask:0xf bank_mask:0xf bound_ctrl:1
	s_nop 0
	v_mul_f32_e32 v2, v2, v26
	v_mul_f32_e32 v31, 0xbfb8aa3b, v31
	v_exp_f32_e32 v31, v31
	v_and_b32_e32 v32, 0xffff0000, v175
	s_waitcnt lgkmcnt(0)
	s_nop 1
	v_add_f32_dpp v21, v21, v21 quad_perm:[2,3,0,1] row_mask:0xf bank_mask:0xf bound_ctrl:1
	s_nop 0
	v_add_f32_e32 v30, 1.0, v31
	v_rcp_f32_e32 v30, v30
	v_lshlrev_b32_e32 v31, 16, v175
	v_mul_f32_e32 v31, 0xbfb8aa3b, v31
	s_waitcnt lgkmcnt(0)
	s_nop 1
	v_add_f32_dpp v21, v21, v21 row_half_mirror row_mask:0xf bank_mask:0xf bound_ctrl:1
	s_nop 0
	v_exp_f32_e32 v31, v31
	v_mul_f32_e32 v32, 0xbfb8aa3b, v32
	v_pk_mul_f32 v[28:29], v[6:7], v[28:29]
	v_exp_f32_e32 v32, v32
	s_waitcnt lgkmcnt(0)
	s_nop 1
	v_add_f32_dpp v21, v21, v21 row_mirror row_mask:0xf bank_mask:0xf bound_ctrl:1
	s_nop 0
	v_add_f32_e32 v31, 1.0, v31
	v_rcp_f32_e32 v31, v31
	v_add_f32_e32 v32, 1.0, v32
	v_rcp_f32_e32 v32, v32
	s_waitcnt lgkmcnt(0)
	s_nop 1
	v_add_f32_dpp v21, v21, v21 row_bcast:15 row_mask:0xa bank_mask:0xf
	s_nop 0
	v_mul_f32_e32 v26, v30, v27
	v_cvt_pk_bf16_f32 v26, v2, v26
	v_mul_f32_e32 v27, v31, v28
	v_mul_f32_e32 v28, v32, v29
	s_waitcnt lgkmcnt(0)
	s_nop 1
	v_add_f32_dpp v2, v21, v21 row_bcast:31 row_mask:0xc bank_mask:0xf
	s_nop 0
	v_readlane_b32 s98, v2, 63
	s_nop 1
	v_mov_b32_e32 v2, s98
	v_fmamk_f32 v2, v2, 0x3b800000, v228
	v_rsq_f32_e32 v244, v2
	s_nop 1
	v_cvt_pk_bf16_f32 v27, v27, v28
	v_add_u32_e32 v28, s10, v15
	s_nop 1
	v_ashrrev_i32_e32 v29, 31, v28
	v_lshlrev_b64 v[28:29], 12, v[28:29]
	v_lshl_add_u64 v[28:29], v[12:13], 0, v[28:29]
	s_nop 1
	global_store_dwordx2 v[28:29], v[26:27], off
	s_nop 1
	s_nop 1
	s_nop 1
	s_nop 1
	s_nop 1
	v_readlane_b32 s2, v247, 52
	s_nop 1
	v_pk_mul_f32 v[26:27], v[24:25], v[24:25]
	v_pk_mul_f32 v[28:29], v[22:23], v[22:23]
	v_mov_b32_e32 v2, v244
	v_pk_mov_b32 v[30:31], v[28:29], v[26:27] op_sel:[1,0]
	v_mov_b32_e32 v29, v27
	v_pk_add_f32 v[26:27], v[30:31], v[28:29]
	v_pk_mul_f32 v[8:9], v[8:9], v[2:3] op_sel_hi:[1,0]
	v_add_f32_e32 v21, v26, v27
	v_pk_mul_f32 v[10:11], v[10:11], v[2:3] op_sel_hi:[1,0]
	v_lshlrev_b32_e32 v2, 16, v180
	s_nop 0
	v_mul_f32_e32 v2, 0xbfb8aa3b, v2
	v_exp_f32_e32 v2, v2
	v_pk_mul_f32 v[8:9], v[4:5], v[8:9]
	v_and_b32_e32 v27, 0xffff0000, v180
	s_waitcnt lgkmcnt(0)
	s_nop 1
	v_add_f32_dpp v21, v21, v21 quad_perm:[1,0,3,2] row_mask:0xf bank_mask:0xf bound_ctrl:1
	v_add_f32_e32 v2, 1.0, v2
	s_nop 0
	v_rcp_f32_e32 v2, v2
	v_mul_f32_e32 v27, 0xbfb8aa3b, v27
	v_exp_f32_e32 v27, v27
	v_and_b32_e32 v28, 0xffff0000, v181
	v_mul_f32_e32 v2, v2, v8
	s_waitcnt lgkmcnt(0)
	s_nop 1
	v_add_f32_dpp v8, v21, v21 quad_perm:[2,3,0,1] row_mask:0xf bank_mask:0xf bound_ctrl:1
	s_nop 0
	v_add_f32_e32 v26, 1.0, v27
	v_lshlrev_b32_e32 v27, 16, v181
	v_mul_f32_e32 v27, 0xbfb8aa3b, v27
	v_mul_f32_e32 v28, 0xbfb8aa3b, v28
	s_waitcnt lgkmcnt(0)
	s_nop 1
	v_add_f32_dpp v8, v8, v8 row_half_mirror row_mask:0xf bank_mask:0xf bound_ctrl:1
	s_nop 0
	v_exp_f32_e32 v27, v27
	v_exp_f32_e32 v28, v28
	v_rcp_f32_e32 v26, v26
	v_pk_mul_f32 v[10:11], v[6:7], v[10:11]
	s_waitcnt lgkmcnt(0)
	s_nop 1
	v_add_f32_dpp v8, v8, v8 row_mirror row_mask:0xf bank_mask:0xf bound_ctrl:1
	s_nop 0
	v_add_f32_e32 v27, 1.0, v27
	v_add_f32_e32 v28, 1.0, v28
	v_rcp_f32_e32 v27, v27
	v_rcp_f32_e32 v28, v28
	s_waitcnt lgkmcnt(0)
	s_nop 1
	v_add_f32_dpp v21, v8, v8 row_bcast:15 row_mask:0xa bank_mask:0xf
	s_nop 0
	v_mul_f32_e32 v8, v26, v9
	v_cvt_pk_bf16_f32 v8, v2, v8
	v_mul_f32_e32 v9, v27, v10
	v_mul_f32_e32 v10, v28, v11
	s_waitcnt lgkmcnt(0)
	s_nop 1
	v_add_f32_dpp v2, v21, v21 row_bcast:31 row_mask:0xc bank_mask:0xf
	s_nop 0
	v_readlane_b32 s98, v2, 63
	s_nop 1
	v_mov_b32_e32 v2, s98
	v_fmamk_f32 v2, v2, 0x3b800000, v228
	v_rsq_f32_e32 v245, v2
	s_nop 1
	v_cvt_pk_bf16_f32 v9, v9, v10
	v_add_u32_e32 v10, s2, v15
	s_nop 1
	v_ashrrev_i32_e32 v11, 31, v10
	v_lshlrev_b64 v[10:11], 12, v[10:11]
	v_lshl_add_u64 v[10:11], v[12:13], 0, v[10:11]
	s_nop 1
	global_store_dwordx2 v[10:11], v[8:9], off
	s_nop 1
	s_nop 1
	s_nop 1
	s_nop 1
	s_nop 1
	s_nop 0
	s_nop 1
	v_mov_b32_e32 v2, v245
	ds_read_b128 v[8:11], v16 offset:6224
	v_pk_mul_f32 v[26:27], v[22:23], v[2:3] op_sel_hi:[1,0]
	v_pk_mul_f32 v[28:29], v[24:25], v[2:3] op_sel_hi:[1,0]
	ds_read_b128 v[22:25], v16 offset:7264
	v_lshlrev_b32_e32 v2, 16, v182
	s_waitcnt lgkmcnt(0)
	v_pk_mul_f32 v[30:31], v[10:11], v[10:11]
	v_pk_mul_f32 v[32:33], v[8:9], v[8:9]
	v_mul_f32_e32 v2, 0xbfb8aa3b, v2
	v_pk_mov_b32 v[34:35], v[32:33], v[30:31] op_sel:[1,0]
	v_mov_b32_e32 v33, v31
	v_pk_add_f32 v[30:31], v[34:35], v[32:33]
	v_exp_f32_e32 v2, v2
	v_add_f32_e32 v16, v30, v31
	s_nop 0
	v_and_b32_e32 v30, 0xffff0000, v182
	v_add_f32_e32 v2, 1.0, v2
	v_mul_f32_e32 v30, 0xbfb8aa3b, v30
	v_rcp_f32_e32 v2, v2
	s_waitcnt lgkmcnt(0)
	s_nop 1
	v_add_f32_dpp v16, v16, v16 quad_perm:[1,0,3,2] row_mask:0xf bank_mask:0xf bound_ctrl:1
	s_nop 0
	v_exp_f32_e32 v30, v30
	v_pk_mul_f32 v[26:27], v[4:5], v[26:27]
	v_and_b32_e32 v31, 0xffff0000, v183
	v_mul_f32_e32 v2, v2, v26
	s_waitcnt lgkmcnt(0)
	s_nop 1
	v_add_f32_dpp v16, v16, v16 quad_perm:[2,3,0,1] row_mask:0xf bank_mask:0xf bound_ctrl:1
	s_nop 0
	v_add_f32_e32 v26, 1.0, v30
	v_rcp_f32_e32 v26, v26
	v_lshlrev_b32_e32 v30, 16, v183
	v_mul_f32_e32 v30, 0xbfb8aa3b, v30
	s_waitcnt lgkmcnt(0)
; __device__ __forceinline__ float fast_sigmoid(float x) { return __builtin_amdgcn_rcpf(1.0f + __expf(-x)); }
; #define LAS __attribute__((address_space(3)))
; __device__ __forceinline__ unsigned pk2(float lo, float hi) { return pg8::cvt_pk_bf16(lo, hi); }
; #define MLC_LOAD_O(IT) do { const int it_ = (IT), h_ = (it_ >> 6) & 7, t0_ = (it_ >> 9) * SEQ + (it_ & 63) * ML_L; \
;         _Pragma("unroll") for (int i = 0; i < 8; ++i) ogw[i] = *(const v2u*)(QKVO + (size_t)(t0_ + 8 * w + i) * 6144 + 4096 + h_ * 256 + 4 * lane); } while (0)
; template <class AT_>
; __device__ __forceinline__ void mlstm_phase_c(const AT_& a, Frame& F, int j) {
;     ...
; #pragma unroll
;         for (int i = 0; i < 8; ++i) { const int tt = 8 * w + i; const f32x4 v = *(const LAS f32x4*)(hbuf + tt * 260 + 4 * lane);
;             const float ss = wave_sum((v.x * v.x + v.y * v.y) + (v.z * v.z + v.w * v.w)); const float rstd = 1.0f / sqrtf(ss * (1.0f / ML_DV) + NORM_EPS);
;             const v2u ow = ogw[i];
;             f32x4 y = v * rstd * gn; y.x *= pg8::fast_sigmoid(bflo(ow.x)); y.y *= pg8::fast_sigmoid(bfhi(ow.x)); y.z *= pg8::fast_sigmoid(bflo(ow.y)); y.w *= pg8::fast_sigmoid(bfhi(ow.y));
;             v2u o; o.x = pk2(y.x, y.y); o.y = pk2(y.z, y.w);
;             *(v2u*)(HS + (size_t)(tok0 + tt) * DM + h * 256 + 4 * lane) = o; }
;         if (has) MLC_LOAD_O(nit);
	s_nop 1
	v_add_f32_dpp v16, v16, v16 row_half_mirror row_mask:0xf bank_mask:0xf bound_ctrl:1
	s_nop 0
	v_mul_f32_e32 v26, v26, v27
	v_exp_f32_e32 v30, v30
	v_cvt_pk_bf16_f32 v26, v2, v26
	v_mul_f32_e32 v31, 0xbfb8aa3b, v31
	s_waitcnt lgkmcnt(0)
	s_nop 1
	v_add_f32_dpp v16, v16, v16 row_mirror row_mask:0xf bank_mask:0xf bound_ctrl:1
	s_nop 0
	v_add_f32_e32 v30, 1.0, v30
	v_rcp_f32_e32 v30, v30
	v_pk_mul_f32 v[28:29], v[6:7], v[28:29]
	v_exp_f32_e32 v31, v31
	s_waitcnt lgkmcnt(0)
	s_nop 1
	v_add_f32_dpp v16, v16, v16 row_bcast:15 row_mask:0xa bank_mask:0xf
	s_nop 0
	v_mul_f32_e32 v27, v30, v28
	v_add_f32_e32 v31, 1.0, v31
	v_rcp_f32_e32 v31, v31
	s_waitcnt lgkmcnt(0)
	s_nop 1
	v_add_f32_dpp v2, v16, v16 row_bcast:31 row_mask:0xc bank_mask:0xf
	s_nop 0
	v_readlane_b32 s98, v2, 63
	s_nop 1
	v_mov_b32_e32 v2, s98
	v_fmamk_f32 v2, v2, 0x3b800000, v228
	v_rsq_f32_e32 v244, v2
	s_nop 1
	v_mul_f32_e32 v28, v31, v29
	v_cvt_pk_bf16_f32 v27, v27, v28
	s_nop 1
	v_add_u32_e32 v28, s11, v15
	v_ashrrev_i32_e32 v29, 31, v28
	v_lshlrev_b64 v[28:29], 12, v[28:29]
	s_nop 1
	v_lshl_add_u64 v[28:29], v[12:13], 0, v[28:29]
	s_nop 1
	global_store_dwordx2 v[28:29], v[26:27], off
	s_nop 0
	s_nop 1
	s_nop 1
	s_nop 1
	v_readlane_b32 s2, v247, 54
	s_nop 1
	v_pk_mul_f32 v[26:27], v[24:25], v[24:25]
	v_pk_mul_f32 v[28:29], v[22:23], v[22:23]
	v_mov_b32_e32 v2, v244
	v_pk_mov_b32 v[30:31], v[28:29], v[26:27] op_sel:[1,0]
	v_mov_b32_e32 v29, v27
	v_pk_add_f32 v[26:27], v[30:31], v[28:29]
	v_pk_mul_f32 v[8:9], v[8:9], v[2:3] op_sel_hi:[1,0]
	v_add_f32_e32 v16, v26, v27
	v_pk_mul_f32 v[10:11], v[10:11], v[2:3] op_sel_hi:[1,0]
	v_lshlrev_b32_e32 v2, 16, v184
	s_nop 0
	v_mul_f32_e32 v2, 0xbfb8aa3b, v2
	v_exp_f32_e32 v2, v2
	v_pk_mul_f32 v[8:9], v[4:5], v[8:9]
	v_pk_mul_f32 v[10:11], v[6:7], v[10:11]
	s_waitcnt lgkmcnt(0)
	s_nop 1
	v_add_f32_dpp v14, v16, v16 quad_perm:[1,0,3,2] row_mask:0xf bank_mask:0xf bound_ctrl:1
	v_add_f32_e32 v2, 1.0, v2
	s_nop 0
	v_rcp_f32_e32 v2, v2
	v_and_b32_e32 v17, 0xffff0000, v184
	v_mul_f32_e32 v17, 0xbfb8aa3b, v17
	v_exp_f32_e32 v17, v17
	v_mul_f32_e32 v2, v2, v8
	s_waitcnt lgkmcnt(0)
	s_nop 1
	v_add_f32_dpp v8, v14, v14 quad_perm:[2,3,0,1] row_mask:0xf bank_mask:0xf bound_ctrl:1
	s_nop 0
	v_add_f32_e32 v16, 1.0, v17
	v_lshlrev_b32_e32 v17, 16, v185
	v_and_b32_e32 v18, 0xffff0000, v185
	v_mul_f32_e32 v17, 0xbfb8aa3b, v17
	s_waitcnt lgkmcnt(0)
	s_nop 1
	v_add_f32_dpp v8, v8, v8 row_half_mirror row_mask:0xf bank_mask:0xf bound_ctrl:1
	s_nop 0
	v_mul_f32_e32 v18, 0xbfb8aa3b, v18
	v_exp_f32_e32 v17, v17
	v_exp_f32_e32 v18, v18
	v_rcp_f32_e32 v16, v16
	s_waitcnt lgkmcnt(0)
	s_nop 1
	v_add_f32_dpp v8, v8, v8 row_mirror row_mask:0xf bank_mask:0xf bound_ctrl:1
	s_nop 0
	v_add_f32_e32 v17, 1.0, v17
	v_add_f32_e32 v18, 1.0, v18
	v_rcp_f32_e32 v17, v17
	v_rcp_f32_e32 v18, v18
	s_waitcnt lgkmcnt(0)
	s_nop 1
	v_add_f32_dpp v14, v8, v8 row_bcast:15 row_mask:0xa bank_mask:0xf
	s_nop 0
	v_mul_f32_e32 v8, v16, v9
	v_cvt_pk_bf16_f32 v8, v2, v8
	v_mul_f32_e32 v9, v17, v10
	v_mul_f32_e32 v10, v18, v11
	s_waitcnt lgkmcnt(0)
	s_nop 1
	v_add_f32_dpp v2, v14, v14 row_bcast:31 row_mask:0xc bank_mask:0xf
	s_nop 0
	v_readlane_b32 s98, v2, 63
	s_nop 1
	v_mov_b32_e32 v2, s98
	v_fmamk_f32 v2, v2, 0x3b800000, v228
	v_rsq_f32_e32 v245, v2
	s_nop 1
	v_cvt_pk_bf16_f32 v9, v9, v10
	v_add_u32_e32 v10, s2, v15
	s_nop 1
	v_ashrrev_i32_e32 v11, 31, v10
	v_lshlrev_b64 v[10:11], 12, v[10:11]
	v_lshl_add_u64 v[10:11], v[12:13], 0, v[10:11]
	s_nop 1
	global_store_dwordx2 v[10:11], v[8:9], off
	s_nop 1
	s_nop 1
	s_nop 1
	s_nop 1
	s_nop 1
	s_nop 0
	s_nop 1
	v_mov_b32_e32 v2, v245
	v_pk_mul_f32 v[10:11], v[24:25], v[2:3] op_sel_hi:[1,0]
	v_pk_mul_f32 v[8:9], v[22:23], v[2:3] op_sel_hi:[1,0]
	v_pk_mul_f32 v[6:7], v[6:7], v[10:11]
	v_and_b32_e32 v10, 0xffff0000, v190
	v_mul_f32_e32 v10, 0xbfb8aa3b, v10
	v_exp_f32_e32 v10, v10
	v_lshlrev_b32_e32 v2, 16, v190
	v_pk_mul_f32 v[4:5], v[4:5], v[8:9]
	v_lshlrev_b32_e32 v9, 16, v191
	v_add_f32_e32 v8, 1.0, v10
	v_and_b32_e32 v10, 0xffff0000, v191
	v_mul_f32_e32 v2, 0xbfb8aa3b, v2
	v_mul_f32_e32 v9, 0xbfb8aa3b, v9
	v_mul_f32_e32 v10, 0xbfb8aa3b, v10
	v_exp_f32_e32 v2, v2
	v_exp_f32_e32 v9, v9
	v_exp_f32_e32 v10, v10
	v_rcp_f32_e32 v8, v8
	v_add_f32_e32 v2, 1.0, v2
	v_add_f32_e32 v9, 1.0, v9
	v_add_f32_e32 v10, 1.0, v10
	v_rcp_f32_e32 v2, v2
	v_rcp_f32_e32 v9, v9
	v_rcp_f32_e32 v10, v10
	v_mul_f32_e32 v2, v2, v4
	v_mul_f32_e32 v4, v8, v5
	v_mul_f32_e32 v5, v9, v6
	v_mul_f32_e32 v6, v10, v7
	v_cvt_pk_bf16_f32 v5, v5, v6
	v_add_u32_e32 v6, s12, v15
	v_ashrrev_i32_e32 v7, 31, v6
	v_lshlrev_b64 v[6:7], 12, v[6:7]
	v_cvt_pk_bf16_f32 v4, v2, v4
	v_lshl_add_u64 v[6:7], v[12:13], 0, v[6:7]
	global_store_dwordx2 v[6:7], v[4:5], off
	s_and_saveexec_b64 s[2:3], s[0:1]
	s_xor_b64 s[0:1], exec, s[2:3]
	v_add_u32_e32 v205, v205, v221
	v_add_u32_e32 v207, v222, v207
	v_add_u32_e32 v209, v223, v209
	s_andn2_saveexec_b64 s[0:1], s[0:1]
	s_cbranch_execz .LBB0_610
	v_and_b32_e32 v2, 0xfffff000, v233
	v_and_b32_e32 v4, 0xfc0, v234
	v_add_u32_e32 v205, v221, v205
	v_add3_u32 v14, v4, s84, v2
	v_and_b32_e32 v2, 0x700, v205
	v_mov_b64_e32 v[4:5], s[80:81]
	v_mad_i64_i32 v[6:7], s[2:3], v14, s14, v[4:5]
	v_lshlrev_b32_e32 v2, 1, v2
	v_lshl_add_u64 v[6:7], v[6:7], 0, v[2:3]
	v_mov_b32_e32 v193, v3
	v_or_b32_e32 v8, 1, v14
	v_lshl_add_u64 v[6:7], v[6:7], 0, v[192:193]
	v_mad_i64_i32 v[8:9], s[2:3], v8, s14, v[4:5]
	v_add_co_u32_e32 v6, vcc, 0x2000, v6
	v_lshl_add_u64 v[8:9], v[8:9], 0, v[2:3]
	v_or_b32_e32 v10, 2, v14
	v_addc_co_u32_e32 v7, vcc, 0, v7, vcc
	v_lshl_add_u64 v[8:9], v[8:9], 0, v[192:193]
	v_mad_i64_i32 v[10:11], s[2:3], v10, s14, v[4:5]
	v_add_co_u32_e32 v8, vcc, 0x2000, v8
	v_lshl_add_u64 v[10:11], v[10:11], 0, v[2:3]
	v_or_b32_e32 v12, 3, v14
	v_addc_co_u32_e32 v9, vcc, 0, v9, vcc
	v_lshl_add_u64 v[10:11], v[10:11], 0, v[192:193]
	v_mad_i64_i32 v[12:13], s[2:3], v12, s14, v[4:5]
	v_add_co_u32_e32 v10, vcc, 0x2000, v10
	v_lshl_add_u64 v[12:13], v[12:13], 0, v[2:3]
	s_nop 0
	v_addc_co_u32_e32 v11, vcc, 0, v11, vcc
	v_lshl_add_u64 v[12:13], v[12:13], 0, v[192:193]
	v_add_co_u32_e32 v12, vcc, 0x2000, v12
	v_mov_b32_e32 v209, v234
	s_nop 0
	v_addc_co_u32_e32 v13, vcc, 0, v13, vcc
	global_load_dwordx2 v[168:169], v[6:7], off
	global_load_dwordx2 v[170:171], v[8:9], off
	global_load_dwordx2 v[172:173], v[10:11], off
	global_load_dwordx2 v[174:175], v[12:13], off
	v_or_b32_e32 v6, 4, v14
	v_mad_i64_i32 v[6:7], s[2:3], v6, s14, v[4:5]
	v_lshl_add_u64 v[6:7], v[6:7], 0, v[2:3]
	v_or_b32_e32 v8, 5, v14
	v_lshl_add_u64 v[6:7], v[6:7], 0, v[192:193]
	v_mad_i64_i32 v[8:9], s[2:3], v8, s14, v[4:5]
	v_add_co_u32_e32 v6, vcc, 0x2000, v6
	v_lshl_add_u64 v[8:9], v[8:9], 0, v[2:3]
	v_or_b32_e32 v10, 6, v14
	v_addc_co_u32_e32 v7, vcc, 0, v7, vcc
	v_lshl_add_u64 v[8:9], v[8:9], 0, v[192:193]
	v_mad_i64_i32 v[10:11], s[2:3], v10, s14, v[4:5]
	v_add_co_u32_e32 v8, vcc, 0x2000, v8
	v_lshl_add_u64 v[10:11], v[10:11], 0, v[2:3]
	v_or_b32_e32 v12, 7, v14
	v_addc_co_u32_e32 v9, vcc, 0, v9, vcc
	v_lshl_add_u64 v[10:11], v[10:11], 0, v[192:193]
	v_mad_i64_i32 v[4:5], s[2:3], v12, s14, v[4:5]
	v_add_co_u32_e32 v10, vcc, 0x2000, v10
	v_lshl_add_u64 v[4:5], v[4:5], 0, v[2:3]
	s_nop 0
	v_addc_co_u32_e32 v11, vcc, 0, v11, vcc
	v_lshl_add_u64 v[4:5], v[4:5], 0, v[192:193]
	v_add_co_u32_e32 v4, vcc, 0x2000, v4
	v_mov_b32_e32 v207, v233
	s_nop 0
	v_addc_co_u32_e32 v5, vcc, 0, v5, vcc
	global_load_dwordx2 v[180:181], v[6:7], off
	global_load_dwordx2 v[182:183], v[8:9], off
	global_load_dwordx2 v[184:185], v[10:11], off
	global_load_dwordx2 v[190:191], v[4:5], off
	s_branch .LBB0_610

; __device__ __forceinline__ float fast_sigmoid(float x) { return __builtin_amdgcn_rcpf(1.0f + __expf(-x)); }
; #define LAS __attribute__((address_space(3)))
; __device__ __forceinline__ unsigned pk2(float lo, float hi) { return pg8::cvt_pk_bf16(lo, hi); }
; #define WG_BAR() do { asm volatile("s_waitcnt lgkmcnt(0)" ::: "memory"); __builtin_amdgcn_s_barrier(); asm volatile("" ::: "memory"); } while (0)
; template <class AT_>
; __device__ __forceinline__ void mlstm_phase_c(const AT_& a, Frame& F, int j) {
;     ...
;         const float inv = 1.0f / fmaxf(fabsf(den), __expf(-mout));
;         WG_BAR();
;         if (has) MLC_LOAD_C(nit);
; #pragma unroll
;         for (int db = 0; db < 2; ++db)
; #pragma unroll
;             for (int g4 = 0; g4 < 4; ++g4) { f32x4 o; o.x = accn[db][4 * g4] * inv; o.y = accn[db][4 * g4 + 1] * inv; o.z = accn[db][4 * g4 + 2] * inv; o.w = accn[db][4 * g4 + 3] * inv;
;                 *(LAS f32x4*)(hbuf + t * 260 + 64 * dq + 32 * db + 8 * g4 + 4 * hh) = o; }
;         WG_BAR();
;         const f32x4 gn = *(const f32x4*)(hgain + h * ML_DV + 4 * lane);
; #pragma unroll
;         for (int i = 0; i < 8; ++i) { const int tt = 8 * w + i; const f32x4 v = *(const LAS f32x4*)(hbuf + tt * 260 + 4 * lane);
;             const float ss = wave_sum((v.x * v.x + v.y * v.y) + (v.z * v.z + v.w * v.w)); const float rstd = 1.0f / sqrtf(ss * (1.0f / ML_DV) + NORM_EPS);
;             const v2u ow = ogw[i];
;             f32x4 y = v * rstd * gn; y.x *= pg8::fast_sigmoid(bflo(ow.x)); y.y *= pg8::fast_sigmoid(bfhi(ow.x)); y.z *= pg8::fast_sigmoid(bflo(ow.y)); y.w *= pg8::fast_sigmoid(bfhi(ow.y));
;             v2u o; o.x = pk2(y.x, y.y); o.y = pk2(y.z, y.w);
;             *(v2u*)(HS + (size_t)(tok0 + tt) * DM + h * 256 + 4 * lane) = o; }
.LBB0_4577:
	s_or_b64 exec, exec, s[74:75]
	v_mul_f32_e32 v2, 0xbfb8aa3b, v237
	v_exp_f32_e32 v2, v2
	v_add_f32_e32 v6, v238, v239
	s_waitcnt lgkmcnt(0)
	v_add_f32_e32 v4, v4, v5
	v_fmac_f32_e32 v6, v166, v4
	v_max_f32_e64 v2, |v6|, v2
	v_div_scale_f32 v4, s[2:3], v2, v2, 1.0
	v_rcp_f32_e32 v5, v4
	v_div_scale_f32 v6, vcc, 1.0, v2, 1.0
	v_and_b32_e32 v26, 0x700, v205
	v_fma_f32 v7, -v4, v5, 1.0
	v_fmac_f32_e32 v5, v7, v5
	v_mul_f32_e32 v7, v6, v5
	v_fma_f32 v8, -v4, v7, v6
	v_fmac_f32_e32 v7, v8, v5
	v_fma_f32 v4, -v4, v7, v6
	v_div_fmas_f32 v4, v4, v5, v7
	v_div_fixup_f32 v2, v4, v2, 1.0
	v_pk_mul_f32 v[4:5], v[36:37], v[2:3] op_sel_hi:[1,0]
	v_pk_mul_f32 v[6:7], v[38:39], v[2:3] op_sel_hi:[1,0]
	ds_write_b128 v227, v[4:7] offset:1024
	v_pk_mul_f32 v[4:5], v[40:41], v[2:3] op_sel_hi:[1,0]
	v_pk_mul_f32 v[6:7], v[42:43], v[2:3] op_sel_hi:[1,0]
	ds_write_b128 v227, v[4:7] offset:1056
	v_pk_mul_f32 v[4:5], v[44:45], v[2:3] op_sel_hi:[1,0]
	v_pk_mul_f32 v[6:7], v[46:47], v[2:3] op_sel_hi:[1,0]
	ds_write_b128 v227, v[4:7] offset:1088
	v_pk_mul_f32 v[4:5], v[48:49], v[2:3] op_sel_hi:[1,0]
	v_pk_mul_f32 v[6:7], v[50:51], v[2:3] op_sel_hi:[1,0]
	ds_write_b128 v227, v[4:7] offset:1120
	v_pk_mul_f32 v[4:5], v[52:53], v[2:3] op_sel_hi:[1,0]
	v_pk_mul_f32 v[6:7], v[54:55], v[2:3] op_sel_hi:[1,0]
	ds_write_b128 v227, v[4:7] offset:1152
	v_pk_mul_f32 v[4:5], v[56:57], v[2:3] op_sel_hi:[1,0]
	v_pk_mul_f32 v[6:7], v[58:59], v[2:3] op_sel_hi:[1,0]
	ds_write_b128 v227, v[4:7] offset:1184
	v_pk_mul_f32 v[4:5], v[60:61], v[2:3] op_sel_hi:[1,0]
	v_pk_mul_f32 v[6:7], v[62:63], v[2:3] op_sel_hi:[1,0]
	ds_write_b128 v227, v[4:7] offset:1216
	v_pk_mul_f32 v[4:5], v[64:65], v[2:3] op_sel_hi:[1,0]
	v_pk_mul_f32 v[6:7], v[66:67], v[2:3] op_sel_hi:[1,0]
	ds_write_b128 v227, v[4:7] offset:1248
	s_waitcnt lgkmcnt(0)
	s_barrier
	v_add_u32_e32 v8, s8, v215
	ds_read_b128 v[22:25], v8 offset:1024
	v_lshlrev_b32_e32 v2, 2, v26
	v_lshl_add_u64 v[4:5], v[190:191], 0, v[2:3]
	v_xor_b32_e32 v2, 1, v226
	v_cmp_lt_i32_e32 vcc, v2, v236
	s_waitcnt lgkmcnt(0)
	v_pk_mul_f32 v[12:13], v[24:25], v[24:25]
	v_pk_mul_f32 v[18:19], v[22:23], v[22:23]
	global_load_dwordx4 v[4:7], v[4:5], off
	v_pk_mov_b32 v[20:21], v[18:19], v[12:13] op_sel:[1,0]
	v_mov_b32_e32 v19, v13
	v_cndmask_b32_e32 v2, v226, v2, vcc
	v_pk_add_f32 v[12:13], v[20:21], v[18:19]
	v_lshlrev_b32_e32 v14, 2, v2
	v_add_f32_e32 v2, v12, v13
	s_nop 0
	v_xor_b32_e32 v13, 2, v226
	v_cmp_lt_i32_e32 vcc, v13, v236
	s_mul_i32 s2, s9, 0x410
	v_add_u32_e32 v16, s2, v215
	v_cndmask_b32_e32 v13, v226, v13, vcc
	v_lshlrev_b32_e32 v17, 2, v13
	s_waitcnt lgkmcnt(0)
	s_nop 1
	v_add_f32_dpp v2, v2, v2 quad_perm:[1,0,3,2] row_mask:0xf bank_mask:0xf bound_ctrl:1
	s_nop 0
	v_xor_b32_e32 v13, 4, v226
	v_cmp_lt_i32_e32 vcc, v13, v236
	ds_read_b128 v[8:11], v16 offset:1024
	s_waitcnt lgkmcnt(0)
	s_nop 1
	v_add_f32_dpp v2, v2, v2 quad_perm:[2,3,0,1] row_mask:0xf bank_mask:0xf bound_ctrl:1
	v_cndmask_b32_e32 v13, v226, v13, vcc
	v_lshlrev_b32_e32 v18, 2, v13
	s_nop 0
	v_xor_b32_e32 v13, 8, v226
	v_cmp_lt_i32_e32 vcc, v13, v236
	s_waitcnt lgkmcnt(0)
	s_nop 1
	v_add_f32_dpp v2, v2, v2 row_half_mirror row_mask:0xf bank_mask:0xf bound_ctrl:1
	v_cndmask_b32_e32 v13, v226, v13, vcc
	v_lshlrev_b32_e32 v19, 2, v13
	s_nop 0
	v_xor_b32_e32 v13, 16, v226
	v_cmp_lt_i32_e32 vcc, v13, v236
	s_waitcnt lgkmcnt(0)
	s_nop 1
	v_add_f32_dpp v2, v2, v2 row_mirror row_mask:0xf bank_mask:0xf bound_ctrl:1
	v_cndmask_b32_e32 v13, v226, v13, vcc
	v_lshlrev_b32_e32 v20, 2, v13
	s_nop 0
	v_and_b32_e32 v13, 0xfc0, v209
	s_waitcnt lgkmcnt(0)
	s_nop 1
	v_add_f32_dpp v2, v2, v2 row_bcast:15 row_mask:0xa bank_mask:0xf
	s_nop 0
	s_waitcnt lgkmcnt(0)
	s_nop 1
	v_add_f32_dpp v2, v2, v2 row_bcast:31 row_mask:0xc bank_mask:0xf
	s_nop 0
	v_readlane_b32 s98, v2, 63
	s_nop 1
	v_mov_b32_e32 v2, s98
	v_fmamk_f32 v2, v2, 0x3b800000, v228
	v_rsq_f32_e32 v244, v2
	s_nop 1
	s_nop 1
	s_nop 1
	s_nop 0
	s_nop 1
	s_nop 0
	s_nop 1
	s_nop 1
	s_nop 1
	s_nop 1
	s_nop 1
	s_movk_i32 s2, 0xf000
	v_lshlrev_b32_e32 v2, 1, v26
	v_and_or_b32 v15, v207, s2, v13
	v_lshl_add_u64 v[12:13], v[194:195], 0, v[2:3]
	s_nop 1
	v_pk_mul_f32 v[26:27], v[10:11], v[10:11]
	v_pk_mul_f32 v[28:29], v[8:9], v[8:9]
	v_mov_b32_e32 v2, v244
	v_pk_mov_b32 v[30:31], v[28:29], v[26:27] op_sel:[1,0]
	v_mov_b32_e32 v29, v27
	v_pk_add_f32 v[26:27], v[30:31], v[28:29]
	v_pk_mul_f32 v[22:23], v[22:23], v[2:3] op_sel_hi:[1,0]
	v_add_f32_e32 v21, v26, v27
	s_nop 0
	v_pk_mul_f32 v[24:25], v[24:25], v[2:3] op_sel_hi:[1,0]
	v_lshlrev_b32_e32 v2, 16, v168
	v_mul_f32_e32 v2, 0xbfb8aa3b, v2
	v_exp_f32_e32 v2, v2
	s_waitcnt lgkmcnt(0)
	s_nop 1
	v_add_f32_dpp v21, v21, v21 quad_perm:[1,0,3,2] row_mask:0xf bank_mask:0xf bound_ctrl:1
	s_nop 0
	s_waitcnt vmcnt(0)
	v_pk_mul_f32 v[22:23], v[4:5], v[22:23]
	v_add_f32_e32 v2, 1.0, v2
	v_rcp_f32_e32 v2, v2
	v_and_b32_e32 v27, 0xffff0000, v168
	s_waitcnt lgkmcnt(0)
	s_nop 1
	v_add_f32_dpp v21, v21, v21 quad_perm:[2,3,0,1] row_mask:0xf bank_mask:0xf bound_ctrl:1
	v_mul_f32_e32 v27, 0xbfb8aa3b, v27
	v_mul_f32_e32 v2, v2, v22
	s_nop 0
	v_exp_f32_e32 v27, v27
	v_and_b32_e32 v28, 0xffff0000, v169
	v_mul_f32_e32 v28, 0xbfb8aa3b, v28
	v_pk_mul_f32 v[24:25], v[6:7], v[24:25]
	s_waitcnt lgkmcnt(0)
	s_nop 1
	v_add_f32_dpp v21, v21, v21 row_half_mirror row_mask:0xf bank_mask:0xf bound_ctrl:1
	s_nop 0
	v_add_f32_e32 v26, 1.0, v27
	v_rcp_f32_e32 v26, v26
	v_lshlrev_b32_e32 v27, 16, v169
	v_mul_f32_e32 v27, 0xbfb8aa3b, v27
	s_waitcnt lgkmcnt(0)
	s_nop 1
	v_add_f32_dpp v21, v21, v21 row_mirror row_mask:0xf bank_mask:0xf bound_ctrl:1
	s_nop 0
	v_exp_f32_e32 v27, v27
	v_exp_f32_e32 v28, v28
	s_waitcnt lgkmcnt(0)
; __device__ __forceinline__ float fast_sigmoid(float x) { return __builtin_amdgcn_rcpf(1.0f + __expf(-x)); }
; #define LAS __attribute__((address_space(3)))
; __device__ __forceinline__ unsigned pk2(float lo, float hi) { return pg8::cvt_pk_bf16(lo, hi); }
; template <class AT_>
; __device__ __forceinline__ void mlstm_phase_c(const AT_& a, Frame& F, int j) {
;     ...
; #pragma unroll
;         for (int i = 0; i < 8; ++i) { const int tt = 8 * w + i; const f32x4 v = *(const LAS f32x4*)(hbuf + tt * 260 + 4 * lane);
;             const float ss = wave_sum((v.x * v.x + v.y * v.y) + (v.z * v.z + v.w * v.w)); const float rstd = 1.0f / sqrtf(ss * (1.0f / ML_DV) + NORM_EPS);
;             const v2u ow = ogw[i];
;             f32x4 y = v * rstd * gn; y.x *= pg8::fast_sigmoid(bflo(ow.x)); y.y *= pg8::fast_sigmoid(bfhi(ow.x)); y.z *= pg8::fast_sigmoid(bflo(ow.y)); y.w *= pg8::fast_sigmoid(bfhi(ow.y));
;             v2u o; o.x = pk2(y.x, y.y); o.y = pk2(y.z, y.w);
;             *(v2u*)(HS + (size_t)(tok0 + tt) * DM + h * 256 + 4 * lane) = o; }
	s_nop 1
	v_add_f32_dpp v21, v21, v21 row_bcast:15 row_mask:0xa bank_mask:0xf
	s_nop 0
	v_mul_f32_e32 v22, v26, v23
	v_cvt_pk_bf16_f32 v22, v2, v22
	v_add_f32_e32 v27, 1.0, v27
	v_rcp_f32_e32 v27, v27
	s_waitcnt lgkmcnt(0)
	s_nop 1
	v_add_f32_dpp v2, v21, v21 row_bcast:31 row_mask:0xc bank_mask:0xf
	s_nop 0
	v_readlane_b32 s98, v2, 63
	s_nop 1
	v_mov_b32_e32 v2, s98
	v_fmamk_f32 v2, v2, 0x3b800000, v228
	v_rsq_f32_e32 v245, v2
	s_nop 1
	v_mul_f32_e32 v23, v27, v24
	v_add_f32_e32 v28, 1.0, v28
	s_nop 1
	v_rcp_f32_e32 v28, v28
	s_nop 1
	v_mul_f32_e32 v24, v28, v25
	s_nop 1
	v_cvt_pk_bf16_f32 v23, v23, v24
	v_add_u32_e32 v24, s84, v15
	s_nop 1
	v_ashrrev_i32_e32 v25, 31, v24
	v_lshlrev_b64 v[24:25], 12, v[24:25]
	s_nop 1
	v_lshl_add_u64 v[24:25], v[12:13], 0, v[24:25]
	global_store_dwordx2 v[24:25], v[22:23], off
	s_nop 1
	v_mov_b32_e32 v2, v245
	v_pk_mul_f32 v[26:27], v[8:9], v[2:3] op_sel_hi:[1,0]
	v_pk_mul_f32 v[28:29], v[10:11], v[2:3] op_sel_hi:[1,0]
	ds_read_b128 v[8:11], v16 offset:2064
	ds_read_b128 v[22:25], v16 offset:3104
	v_lshlrev_b32_e32 v2, 16, v170
	v_mul_f32_e32 v2, 0xbfb8aa3b, v2
	v_exp_f32_e32 v2, v2
	s_waitcnt lgkmcnt(0)
	v_pk_mul_f32 v[30:31], v[10:11], v[10:11]
	v_pk_mul_f32 v[32:33], v[8:9], v[8:9]
	v_pk_mul_f32 v[26:27], v[4:5], v[26:27]
	v_pk_mov_b32 v[34:35], v[32:33], v[30:31] op_sel:[1,0]
	v_mov_b32_e32 v33, v31
	v_pk_add_f32 v[30:31], v[34:35], v[32:33]
	v_add_f32_e32 v2, 1.0, v2
	v_add_f32_e32 v21, v30, v31
	s_nop 0
	v_rcp_f32_e32 v2, v2
	v_and_b32_e32 v31, 0xffff0000, v170
	v_mul_f32_e32 v31, 0xbfb8aa3b, v31
	v_exp_f32_e32 v31, v31
	s_waitcnt lgkmcnt(0)
	s_nop 1
	v_add_f32_dpp v21, v21, v21 quad_perm:[1,0,3,2] row_mask:0xf bank_mask:0xf bound_ctrl:1
	s_nop 0
	v_mul_f32_e32 v2, v2, v26
	v_and_b32_e32 v32, 0xffff0000, v171
	v_mul_f32_e32 v32, 0xbfb8aa3b, v32
	v_pk_mul_f32 v[28:29], v[6:7], v[28:29]
	s_waitcnt lgkmcnt(0)
	s_nop 1
	v_add_f32_dpp v21, v21, v21 quad_perm:[2,3,0,1] row_mask:0xf bank_mask:0xf bound_ctrl:1
	s_nop 0
	v_add_f32_e32 v30, 1.0, v31
	v_rcp_f32_e32 v30, v30
	v_lshlrev_b32_e32 v31, 16, v171
	v_mul_f32_e32 v31, 0xbfb8aa3b, v31
	s_waitcnt lgkmcnt(0)
	s_nop 1
	v_add_f32_dpp v21, v21, v21 row_half_mirror row_mask:0xf bank_mask:0xf bound_ctrl:1
	s_nop 0
	v_exp_f32_e32 v31, v31
	v_exp_f32_e32 v32, v32
	s_waitcnt lgkmcnt(0)
	s_nop 1
	v_add_f32_dpp v21, v21, v21 row_mirror row_mask:0xf bank_mask:0xf bound_ctrl:1
	s_nop 0
	v_add_f32_e32 v31, 1.0, v31
	v_rcp_f32_e32 v31, v31
	v_add_f32_e32 v32, 1.0, v32
	v_rcp_f32_e32 v32, v32
	s_waitcnt lgkmcnt(0)
	s_nop 1
	v_add_f32_dpp v21, v21, v21 row_bcast:15 row_mask:0xa bank_mask:0xf
	s_nop 0
	v_mul_f32_e32 v26, v30, v27
	v_cvt_pk_bf16_f32 v26, v2, v26
	v_mul_f32_e32 v27, v31, v28
	v_mul_f32_e32 v28, v32, v29
	s_waitcnt lgkmcnt(0)
	s_nop 1
	v_add_f32_dpp v2, v21, v21 row_bcast:31 row_mask:0xc bank_mask:0xf
	s_nop 0
	v_readlane_b32 s98, v2, 63
	s_nop 1
	v_mov_b32_e32 v2, s98
	v_fmamk_f32 v2, v2, 0x3b800000, v228
	v_rsq_f32_e32 v244, v2
	s_nop 1
	v_cvt_pk_bf16_f32 v27, v27, v28
	v_add_u32_e32 v28, s9, v15
	s_nop 1
	v_ashrrev_i32_e32 v29, 31, v28
	v_lshlrev_b64 v[28:29], 12, v[28:29]
	v_lshl_add_u64 v[28:29], v[12:13], 0, v[28:29]
	s_nop 1
	global_store_dwordx2 v[28:29], v[26:27], off
	s_nop 1
	s_nop 1
	s_nop 1
	s_nop 1
	s_nop 1
	s_nop 0
	s_nop 1
	v_pk_mul_f32 v[26:27], v[24:25], v[24:25]
	v_pk_mul_f32 v[28:29], v[22:23], v[22:23]
	v_mov_b32_e32 v2, v244
	v_pk_mov_b32 v[30:31], v[28:29], v[26:27] op_sel:[1,0]
	v_mov_b32_e32 v29, v27
	v_pk_add_f32 v[26:27], v[30:31], v[28:29]
	v_pk_mul_f32 v[8:9], v[8:9], v[2:3] op_sel_hi:[1,0]
	v_add_f32_e32 v21, v26, v27
	v_pk_mul_f32 v[10:11], v[10:11], v[2:3] op_sel_hi:[1,0]
	v_lshlrev_b32_e32 v2, 16, v172
	s_nop 0
	v_mul_f32_e32 v2, 0xbfb8aa3b, v2
	v_exp_f32_e32 v2, v2
	v_pk_mul_f32 v[8:9], v[4:5], v[8:9]
	v_and_b32_e32 v27, 0xffff0000, v172
	s_waitcnt lgkmcnt(0)
	s_nop 1
	v_add_f32_dpp v21, v21, v21 quad_perm:[1,0,3,2] row_mask:0xf bank_mask:0xf bound_ctrl:1
	v_add_f32_e32 v2, 1.0, v2
	s_nop 0
	v_rcp_f32_e32 v2, v2
	v_mul_f32_e32 v27, 0xbfb8aa3b, v27
	v_exp_f32_e32 v27, v27
	v_and_b32_e32 v28, 0xffff0000, v173
	v_mul_f32_e32 v2, v2, v8
	s_waitcnt lgkmcnt(0)
	s_nop 1
	v_add_f32_dpp v8, v21, v21 quad_perm:[2,3,0,1] row_mask:0xf bank_mask:0xf bound_ctrl:1
	s_nop 0
	v_add_f32_e32 v26, 1.0, v27
	v_lshlrev_b32_e32 v27, 16, v173
	v_mul_f32_e32 v27, 0xbfb8aa3b, v27
	v_mul_f32_e32 v28, 0xbfb8aa3b, v28
	s_waitcnt lgkmcnt(0)
	s_nop 1
	v_add_f32_dpp v8, v8, v8 row_half_mirror row_mask:0xf bank_mask:0xf bound_ctrl:1
	s_nop 0
	v_exp_f32_e32 v27, v27
	v_exp_f32_e32 v28, v28
	v_rcp_f32_e32 v26, v26
	v_pk_mul_f32 v[10:11], v[6:7], v[10:11]
	s_waitcnt lgkmcnt(0)
	s_nop 1
	v_add_f32_dpp v8, v8, v8 row_mirror row_mask:0xf bank_mask:0xf bound_ctrl:1
	s_nop 0
	v_add_f32_e32 v27, 1.0, v27
	v_add_f32_e32 v28, 1.0, v28
	v_rcp_f32_e32 v27, v27
	v_rcp_f32_e32 v28, v28
	s_waitcnt lgkmcnt(0)
	s_nop 1
	v_add_f32_dpp v21, v8, v8 row_bcast:15 row_mask:0xa bank_mask:0xf
	s_nop 0
	v_mul_f32_e32 v8, v26, v9
	v_cvt_pk_bf16_f32 v8, v2, v8
	v_mul_f32_e32 v9, v27, v10
	v_mul_f32_e32 v10, v28, v11
	s_waitcnt lgkmcnt(0)
	s_nop 1
	v_add_f32_dpp v2, v21, v21 row_bcast:31 row_mask:0xc bank_mask:0xf
	s_nop 0
	v_readlane_b32 s98, v2, 63
	s_nop 1
	v_mov_b32_e32 v2, s98
	v_fmamk_f32 v2, v2, 0x3b800000, v228
	v_rsq_f32_e32 v245, v2
	s_nop 1
	v_cvt_pk_bf16_f32 v9, v9, v10
	v_add_u32_e32 v10, s90, v15
	s_nop 1
	v_ashrrev_i32_e32 v11, 31, v10
	v_lshlrev_b64 v[10:11], 12, v[10:11]
	v_lshl_add_u64 v[10:11], v[12:13], 0, v[10:11]
	s_nop 1
	global_store_dwordx2 v[10:11], v[8:9], off
	s_nop 1
	s_nop 1
	s_nop 1
	s_nop 1
	s_nop 1
	s_nop 0
	s_nop 1
	v_mov_b32_e32 v2, v245
	ds_read_b128 v[8:11], v16 offset:4144
	v_pk_mul_f32 v[26:27], v[22:23], v[2:3] op_sel_hi:[1,0]
	v_pk_mul_f32 v[28:29], v[24:25], v[2:3] op_sel_hi:[1,0]
	ds_read_b128 v[22:25], v16 offset:5184
	v_lshlrev_b32_e32 v2, 16, v174
	s_waitcnt lgkmcnt(0)
; __device__ __forceinline__ float fast_sigmoid(float x) { return __builtin_amdgcn_rcpf(1.0f + __expf(-x)); }
; #define LAS __attribute__((address_space(3)))
; __device__ __forceinline__ unsigned pk2(float lo, float hi) { return pg8::cvt_pk_bf16(lo, hi); }
; template <class AT_>
; __device__ __forceinline__ void mlstm_phase_c(const AT_& a, Frame& F, int j) {
;     ...
; #pragma unroll
;         for (int i = 0; i < 8; ++i) { const int tt = 8 * w + i; const f32x4 v = *(const LAS f32x4*)(hbuf + tt * 260 + 4 * lane);
;             const float ss = wave_sum((v.x * v.x + v.y * v.y) + (v.z * v.z + v.w * v.w)); const float rstd = 1.0f / sqrtf(ss * (1.0f / ML_DV) + NORM_EPS);
;             const v2u ow = ogw[i];
;             f32x4 y = v * rstd * gn; y.x *= pg8::fast_sigmoid(bflo(ow.x)); y.y *= pg8::fast_sigmoid(bfhi(ow.x)); y.z *= pg8::fast_sigmoid(bflo(ow.y)); y.w *= pg8::fast_sigmoid(bfhi(ow.y));
;             v2u o; o.x = pk2(y.x, y.y); o.y = pk2(y.z, y.w);
;             *(v2u*)(HS + (size_t)(tok0 + tt) * DM + h * 256 + 4 * lane) = o; }
	v_pk_mul_f32 v[30:31], v[10:11], v[10:11]
	v_pk_mul_f32 v[32:33], v[8:9], v[8:9]
	v_mul_f32_e32 v2, 0xbfb8aa3b, v2
	v_pk_mov_b32 v[34:35], v[32:33], v[30:31] op_sel:[1,0]
	v_mov_b32_e32 v33, v31
	v_pk_add_f32 v[30:31], v[34:35], v[32:33]
	v_exp_f32_e32 v2, v2
	v_add_f32_e32 v21, v30, v31
	s_nop 0
	v_pk_mul_f32 v[26:27], v[4:5], v[26:27]
	v_add_f32_e32 v2, 1.0, v2
	v_rcp_f32_e32 v2, v2
	v_and_b32_e32 v31, 0xffff0000, v174
	s_waitcnt lgkmcnt(0)
	s_nop 1
	v_add_f32_dpp v21, v21, v21 quad_perm:[1,0,3,2] row_mask:0xf bank_mask:0xf bound_ctrl:1
	s_nop 0
	v_mul_f32_e32 v2, v2, v26
	v_mul_f32_e32 v31, 0xbfb8aa3b, v31
	v_exp_f32_e32 v31, v31
	v_and_b32_e32 v32, 0xffff0000, v175
	s_waitcnt lgkmcnt(0)
	s_nop 1
	v_add_f32_dpp v21, v21, v21 quad_perm:[2,3,0,1] row_mask:0xf bank_mask:0xf bound_ctrl:1
	s_nop 0
	v_add_f32_e32 v30, 1.0, v31
	v_rcp_f32_e32 v30, v30
	v_lshlrev_b32_e32 v31, 16, v175
	v_mul_f32_e32 v31, 0xbfb8aa3b, v31
	s_waitcnt lgkmcnt(0)
	s_nop 1
	v_add_f32_dpp v21, v21, v21 row_half_mirror row_mask:0xf bank_mask:0xf bound_ctrl:1
	s_nop 0
	v_exp_f32_e32 v31, v31
	v_mul_f32_e32 v32, 0xbfb8aa3b, v32
	v_pk_mul_f32 v[28:29], v[6:7], v[28:29]
	v_exp_f32_e32 v32, v32
	s_waitcnt lgkmcnt(0)
	s_nop 1
	v_add_f32_dpp v21, v21, v21 row_mirror row_mask:0xf bank_mask:0xf bound_ctrl:1
	s_nop 0
	v_add_f32_e32 v31, 1.0, v31
	v_rcp_f32_e32 v31, v31
	v_add_f32_e32 v32, 1.0, v32
	v_rcp_f32_e32 v32, v32
	s_waitcnt lgkmcnt(0)
	s_nop 1
	v_add_f32_dpp v21, v21, v21 row_bcast:15 row_mask:0xa bank_mask:0xf
	s_nop 0
	v_mul_f32_e32 v26, v30, v27
	v_cvt_pk_bf16_f32 v26, v2, v26
	v_mul_f32_e32 v27, v31, v28
	v_mul_f32_e32 v28, v32, v29
	s_waitcnt lgkmcnt(0)
	s_nop 1
	v_add_f32_dpp v2, v21, v21 row_bcast:31 row_mask:0xc bank_mask:0xf
	s_nop 0
	v_readlane_b32 s98, v2, 63
	s_nop 1
	v_mov_b32_e32 v2, s98
	v_fmamk_f32 v2, v2, 0x3b800000, v228
	v_rsq_f32_e32 v244, v2
	s_nop 1
	v_cvt_pk_bf16_f32 v27, v27, v28
	v_add_u32_e32 v28, s10, v15
	s_nop 1
	v_ashrrev_i32_e32 v29, 31, v28
	v_lshlrev_b64 v[28:29], 12, v[28:29]
	v_lshl_add_u64 v[28:29], v[12:13], 0, v[28:29]
	s_nop 1
	global_store_dwordx2 v[28:29], v[26:27], off
	s_nop 1
	s_nop 1
	s_nop 1
	s_nop 1
	s_nop 1
	v_readlane_b32 s2, v247, 52
	s_nop 1
	v_pk_mul_f32 v[26:27], v[24:25], v[24:25]
	v_pk_mul_f32 v[28:29], v[22:23], v[22:23]
	v_mov_b32_e32 v2, v244
	v_pk_mov_b32 v[30:31], v[28:29], v[26:27] op_sel:[1,0]
	v_mov_b32_e32 v29, v27
	v_pk_add_f32 v[26:27], v[30:31], v[28:29]
	v_pk_mul_f32 v[8:9], v[8:9], v[2:3] op_sel_hi:[1,0]
	v_add_f32_e32 v21, v26, v27
	v_pk_mul_f32 v[10:11], v[10:11], v[2:3] op_sel_hi:[1,0]
	v_lshlrev_b32_e32 v2, 16, v180
	s_nop 0
	v_mul_f32_e32 v2, 0xbfb8aa3b, v2
	v_exp_f32_e32 v2, v2
	v_pk_mul_f32 v[8:9], v[4:5], v[8:9]
	v_and_b32_e32 v27, 0xffff0000, v180
	s_waitcnt lgkmcnt(0)
	s_nop 1
	v_add_f32_dpp v21, v21, v21 quad_perm:[1,0,3,2] row_mask:0xf bank_mask:0xf bound_ctrl:1
	v_add_f32_e32 v2, 1.0, v2
	s_nop 0
	v_rcp_f32_e32 v2, v2
	v_mul_f32_e32 v27, 0xbfb8aa3b, v27
	v_exp_f32_e32 v27, v27
	v_and_b32_e32 v28, 0xffff0000, v181
	v_mul_f32_e32 v2, v2, v8
	s_waitcnt lgkmcnt(0)
	s_nop 1
	v_add_f32_dpp v8, v21, v21 quad_perm:[2,3,0,1] row_mask:0xf bank_mask:0xf bound_ctrl:1
	s_nop 0
	v_add_f32_e32 v26, 1.0, v27
	v_lshlrev_b32_e32 v27, 16, v181
	v_mul_f32_e32 v27, 0xbfb8aa3b, v27
	v_mul_f32_e32 v28, 0xbfb8aa3b, v28
	s_waitcnt lgkmcnt(0)
	s_nop 1
	v_add_f32_dpp v8, v8, v8 row_half_mirror row_mask:0xf bank_mask:0xf bound_ctrl:1
	s_nop 0
	v_exp_f32_e32 v27, v27
	v_exp_f32_e32 v28, v28
	v_rcp_f32_e32 v26, v26
	v_pk_mul_f32 v[10:11], v[6:7], v[10:11]
	s_waitcnt lgkmcnt(0)
	s_nop 1
	v_add_f32_dpp v8, v8, v8 row_mirror row_mask:0xf bank_mask:0xf bound_ctrl:1
	s_nop 0
	v_add_f32_e32 v27, 1.0, v27
	v_add_f32_e32 v28, 1.0, v28
	v_rcp_f32_e32 v27, v27
	v_rcp_f32_e32 v28, v28
	s_waitcnt lgkmcnt(0)
	s_nop 1
	v_add_f32_dpp v21, v8, v8 row_bcast:15 row_mask:0xa bank_mask:0xf
	s_nop 0
	v_mul_f32_e32 v8, v26, v9
	v_cvt_pk_bf16_f32 v8, v2, v8
	v_mul_f32_e32 v9, v27, v10
	v_mul_f32_e32 v10, v28, v11
	s_waitcnt lgkmcnt(0)
	s_nop 1
	v_add_f32_dpp v2, v21, v21 row_bcast:31 row_mask:0xc bank_mask:0xf
	s_nop 0
	v_readlane_b32 s98, v2, 63
	s_nop 1
	v_mov_b32_e32 v2, s98
	v_fmamk_f32 v2, v2, 0x3b800000, v228
	v_rsq_f32_e32 v245, v2
	s_nop 1
	v_cvt_pk_bf16_f32 v9, v9, v10
	v_add_u32_e32 v10, s2, v15
	s_nop 1
	v_ashrrev_i32_e32 v11, 31, v10
	v_lshlrev_b64 v[10:11], 12, v[10:11]
	v_lshl_add_u64 v[10:11], v[12:13], 0, v[10:11]
	s_nop 1
	global_store_dwordx2 v[10:11], v[8:9], off
	s_nop 1
	s_nop 1
	s_nop 1
	s_nop 1
	s_nop 1
	s_nop 0
	s_nop 1
	v_mov_b32_e32 v2, v245
	ds_read_b128 v[8:11], v16 offset:6224
	v_pk_mul_f32 v[26:27], v[22:23], v[2:3] op_sel_hi:[1,0]
	v_pk_mul_f32 v[28:29], v[24:25], v[2:3] op_sel_hi:[1,0]
	ds_read_b128 v[22:25], v16 offset:7264
	v_lshlrev_b32_e32 v2, 16, v182
	s_waitcnt lgkmcnt(0)
	v_pk_mul_f32 v[30:31], v[10:11], v[10:11]
	v_pk_mul_f32 v[32:33], v[8:9], v[8:9]
	v_mul_f32_e32 v2, 0xbfb8aa3b, v2
	v_pk_mov_b32 v[34:35], v[32:33], v[30:31] op_sel:[1,0]
	v_mov_b32_e32 v33, v31
	v_pk_add_f32 v[30:31], v[34:35], v[32:33]
	v_exp_f32_e32 v2, v2
	v_add_f32_e32 v16, v30, v31
	s_nop 0
	v_and_b32_e32 v30, 0xffff0000, v182
	v_add_f32_e32 v2, 1.0, v2
	v_mul_f32_e32 v30, 0xbfb8aa3b, v30
	v_rcp_f32_e32 v2, v2
	s_waitcnt lgkmcnt(0)
	s_nop 1
	v_add_f32_dpp v16, v16, v16 quad_perm:[1,0,3,2] row_mask:0xf bank_mask:0xf bound_ctrl:1
	s_nop 0
	v_exp_f32_e32 v30, v30
	v_pk_mul_f32 v[26:27], v[4:5], v[26:27]
	v_and_b32_e32 v31, 0xffff0000, v183
	v_mul_f32_e32 v2, v2, v26
	s_waitcnt lgkmcnt(0)
	s_nop 1
	v_add_f32_dpp v16, v16, v16 quad_perm:[2,3,0,1] row_mask:0xf bank_mask:0xf bound_ctrl:1
	s_nop 0
	v_add_f32_e32 v26, 1.0, v30
	v_rcp_f32_e32 v26, v26
	v_lshlrev_b32_e32 v30, 16, v183
	v_mul_f32_e32 v30, 0xbfb8aa3b, v30
	s_waitcnt lgkmcnt(0)
; __device__ __forceinline__ float fast_sigmoid(float x) { return __builtin_amdgcn_rcpf(1.0f + __expf(-x)); }
; #define LAS __attribute__((address_space(3)))
; __device__ __forceinline__ unsigned pk2(float lo, float hi) { return pg8::cvt_pk_bf16(lo, hi); }
; #define MLC_LOAD_O(IT) do { const int it_ = (IT), h_ = (it_ >> 6) & 7, t0_ = (it_ >> 9) * SEQ + (it_ & 63) * ML_L; \
;         _Pragma("unroll") for (int i = 0; i < 8; ++i) ogw[i] = *(const v2u*)(QKVO + (size_t)(t0_ + 8 * w + i) * 6144 + 4096 + h_ * 256 + 4 * lane); } while (0)
; template <class AT_>
; __device__ __forceinline__ void mlstm_phase_c(const AT_& a, Frame& F, int j) {
;     ...
; #pragma unroll
;         for (int i = 0; i < 8; ++i) { const int tt = 8 * w + i; const f32x4 v = *(const LAS f32x4*)(hbuf + tt * 260 + 4 * lane);
;             const float ss = wave_sum((v.x * v.x + v.y * v.y) + (v.z * v.z + v.w * v.w)); const float rstd = 1.0f / sqrtf(ss * (1.0f / ML_DV) + NORM_EPS);
;             const v2u ow = ogw[i];
;             f32x4 y = v * rstd * gn; y.x *= pg8::fast_sigmoid(bflo(ow.x)); y.y *= pg8::fast_sigmoid(bfhi(ow.x)); y.z *= pg8::fast_sigmoid(bflo(ow.y)); y.w *= pg8::fast_sigmoid(bfhi(ow.y));
;             v2u o; o.x = pk2(y.x, y.y); o.y = pk2(y.z, y.w);
;             *(v2u*)(HS + (size_t)(tok0 + tt) * DM + h * 256 + 4 * lane) = o; }
;         if (has) MLC_LOAD_O(nit);
	s_nop 1
	v_add_f32_dpp v16, v16, v16 row_half_mirror row_mask:0xf bank_mask:0xf bound_ctrl:1
	s_nop 0
	v_mul_f32_e32 v26, v26, v27
	v_exp_f32_e32 v30, v30
	v_cvt_pk_bf16_f32 v26, v2, v26
	v_mul_f32_e32 v31, 0xbfb8aa3b, v31
	s_waitcnt lgkmcnt(0)
	s_nop 1
	v_add_f32_dpp v16, v16, v16 row_mirror row_mask:0xf bank_mask:0xf bound_ctrl:1
	s_nop 0
	v_add_f32_e32 v30, 1.0, v30
	v_rcp_f32_e32 v30, v30
	v_pk_mul_f32 v[28:29], v[6:7], v[28:29]
	v_exp_f32_e32 v31, v31
	s_waitcnt lgkmcnt(0)
	s_nop 1
	v_add_f32_dpp v16, v16, v16 row_bcast:15 row_mask:0xa bank_mask:0xf
	s_nop 0
	v_mul_f32_e32 v27, v30, v28
	v_add_f32_e32 v31, 1.0, v31
	v_rcp_f32_e32 v31, v31
	s_waitcnt lgkmcnt(0)
	s_nop 1
	v_add_f32_dpp v2, v16, v16 row_bcast:31 row_mask:0xc bank_mask:0xf
	s_nop 0
	v_readlane_b32 s98, v2, 63
	s_nop 1
	v_mov_b32_e32 v2, s98
	v_fmamk_f32 v2, v2, 0x3b800000, v228
	v_rsq_f32_e32 v244, v2
	s_nop 1
	v_mul_f32_e32 v28, v31, v29
	v_cvt_pk_bf16_f32 v27, v27, v28
	s_nop 1
	v_add_u32_e32 v28, s11, v15
	v_ashrrev_i32_e32 v29, 31, v28
	v_lshlrev_b64 v[28:29], 12, v[28:29]
	s_nop 1
	v_lshl_add_u64 v[28:29], v[12:13], 0, v[28:29]
	s_nop 1
	global_store_dwordx2 v[28:29], v[26:27], off
	s_nop 0
	s_nop 1
	s_nop 1
	s_nop 1
	v_readlane_b32 s2, v247, 54
	s_nop 1
	v_pk_mul_f32 v[26:27], v[24:25], v[24:25]
	v_pk_mul_f32 v[28:29], v[22:23], v[22:23]
	v_mov_b32_e32 v2, v244
	v_pk_mov_b32 v[30:31], v[28:29], v[26:27] op_sel:[1,0]
	v_mov_b32_e32 v29, v27
	v_pk_add_f32 v[26:27], v[30:31], v[28:29]
	v_pk_mul_f32 v[8:9], v[8:9], v[2:3] op_sel_hi:[1,0]
	v_add_f32_e32 v16, v26, v27
	v_pk_mul_f32 v[10:11], v[10:11], v[2:3] op_sel_hi:[1,0]
	v_lshlrev_b32_e32 v2, 16, v184
	s_nop 0
	v_mul_f32_e32 v2, 0xbfb8aa3b, v2
	v_exp_f32_e32 v2, v2
	v_pk_mul_f32 v[8:9], v[4:5], v[8:9]
	v_pk_mul_f32 v[10:11], v[6:7], v[10:11]
	s_waitcnt lgkmcnt(0)
	s_nop 1
	v_add_f32_dpp v14, v16, v16 quad_perm:[1,0,3,2] row_mask:0xf bank_mask:0xf bound_ctrl:1
	v_add_f32_e32 v2, 1.0, v2
	s_nop 0
	v_rcp_f32_e32 v2, v2
	v_and_b32_e32 v17, 0xffff0000, v184
	v_mul_f32_e32 v17, 0xbfb8aa3b, v17
	v_exp_f32_e32 v17, v17
	v_mul_f32_e32 v2, v2, v8
	s_waitcnt lgkmcnt(0)
	s_nop 1
	v_add_f32_dpp v8, v14, v14 quad_perm:[2,3,0,1] row_mask:0xf bank_mask:0xf bound_ctrl:1
	s_nop 0
	v_add_f32_e32 v16, 1.0, v17
	v_lshlrev_b32_e32 v17, 16, v185
	v_and_b32_e32 v18, 0xffff0000, v185
	v_mul_f32_e32 v17, 0xbfb8aa3b, v17
	s_waitcnt lgkmcnt(0)
	s_nop 1
	v_add_f32_dpp v8, v8, v8 row_half_mirror row_mask:0xf bank_mask:0xf bound_ctrl:1
	s_nop 0
	v_mul_f32_e32 v18, 0xbfb8aa3b, v18
	v_exp_f32_e32 v17, v17
	v_exp_f32_e32 v18, v18
	v_rcp_f32_e32 v16, v16
	s_waitcnt lgkmcnt(0)
	s_nop 1
	v_add_f32_dpp v8, v8, v8 row_mirror row_mask:0xf bank_mask:0xf bound_ctrl:1
	s_nop 0
	v_add_f32_e32 v17, 1.0, v17
	v_add_f32_e32 v18, 1.0, v18
	v_rcp_f32_e32 v17, v17
	v_rcp_f32_e32 v18, v18
	s_waitcnt lgkmcnt(0)
	s_nop 1
	v_add_f32_dpp v14, v8, v8 row_bcast:15 row_mask:0xa bank_mask:0xf
	s_nop 0
	v_mul_f32_e32 v8, v16, v9
	v_cvt_pk_bf16_f32 v8, v2, v8
	v_mul_f32_e32 v9, v17, v10
	v_mul_f32_e32 v10, v18, v11
	s_waitcnt lgkmcnt(0)
	s_nop 1
	v_add_f32_dpp v2, v14, v14 row_bcast:31 row_mask:0xc bank_mask:0xf
	s_nop 0
	v_readlane_b32 s98, v2, 63
	s_nop 1
	v_mov_b32_e32 v2, s98
	v_fmamk_f32 v2, v2, 0x3b800000, v228
	v_rsq_f32_e32 v245, v2
	s_nop 1
	v_cvt_pk_bf16_f32 v9, v9, v10
	v_add_u32_e32 v10, s2, v15
	s_nop 1
	v_ashrrev_i32_e32 v11, 31, v10
	v_lshlrev_b64 v[10:11], 12, v[10:11]
	v_lshl_add_u64 v[10:11], v[12:13], 0, v[10:11]
	s_nop 1
	global_store_dwordx2 v[10:11], v[8:9], off
	s_nop 1
	s_nop 1
	s_nop 1
	s_nop 1
	s_nop 1
	s_nop 0
	s_nop 1
	v_mov_b32_e32 v2, v245
	v_pk_mul_f32 v[10:11], v[24:25], v[2:3] op_sel_hi:[1,0]
	v_pk_mul_f32 v[8:9], v[22:23], v[2:3] op_sel_hi:[1,0]
	v_pk_mul_f32 v[6:7], v[6:7], v[10:11]
	v_and_b32_e32 v10, 0xffff0000, v188
	v_mul_f32_e32 v10, 0xbfb8aa3b, v10
	v_exp_f32_e32 v10, v10
	v_lshlrev_b32_e32 v2, 16, v188
	v_pk_mul_f32 v[4:5], v[4:5], v[8:9]
	v_lshlrev_b32_e32 v9, 16, v189
	v_add_f32_e32 v8, 1.0, v10
	v_and_b32_e32 v10, 0xffff0000, v189
	v_mul_f32_e32 v2, 0xbfb8aa3b, v2
	v_mul_f32_e32 v9, 0xbfb8aa3b, v9
	v_mul_f32_e32 v10, 0xbfb8aa3b, v10
	v_exp_f32_e32 v2, v2
	v_exp_f32_e32 v9, v9
	v_exp_f32_e32 v10, v10
	v_rcp_f32_e32 v8, v8
	v_add_f32_e32 v2, 1.0, v2
	v_add_f32_e32 v9, 1.0, v9
	v_add_f32_e32 v10, 1.0, v10
	v_rcp_f32_e32 v2, v2
	v_rcp_f32_e32 v9, v9
	v_rcp_f32_e32 v10, v10
	v_mul_f32_e32 v2, v2, v4
	v_mul_f32_e32 v4, v8, v5
	v_mul_f32_e32 v5, v9, v6
	v_mul_f32_e32 v6, v10, v7
	v_cvt_pk_bf16_f32 v5, v5, v6
	v_add_u32_e32 v6, s12, v15
	v_ashrrev_i32_e32 v7, 31, v6
	v_lshlrev_b64 v[6:7], 12, v[6:7]
	v_cvt_pk_bf16_f32 v4, v2, v4
	v_lshl_add_u64 v[6:7], v[12:13], 0, v[6:7]
	global_store_dwordx2 v[6:7], v[4:5], off
	s_and_saveexec_b64 s[2:3], s[0:1]
	s_xor_b64 s[0:1], exec, s[2:3]
	v_add_u32_e32 v205, v205, v221
	v_add_u32_e32 v207, v222, v207
	v_add_u32_e32 v209, v223, v209
	s_andn2_saveexec_b64 s[0:1], s[0:1]
	s_cbranch_execz .LBB0_4543
	v_and_b32_e32 v2, 0xfffff000, v233
	v_and_b32_e32 v4, 0xfc0, v234
	v_add_u32_e32 v205, v221, v205
	v_add3_u32 v14, v4, s84, v2
	v_and_b32_e32 v2, 0x700, v205
	v_mov_b64_e32 v[4:5], s[80:81]
	v_mad_i64_i32 v[6:7], s[2:3], v14, s14, v[4:5]
	v_lshlrev_b32_e32 v2, 1, v2
	v_lshl_add_u64 v[6:7], v[6:7], 0, v[2:3]
	v_mov_b32_e32 v193, v3
	v_or_b32_e32 v8, 1, v14
	v_lshl_add_u64 v[6:7], v[6:7], 0, v[192:193]
	v_mad_i64_i32 v[8:9], s[2:3], v8, s14, v[4:5]
	v_add_co_u32_e32 v6, vcc, 0x2000, v6
	v_lshl_add_u64 v[8:9], v[8:9], 0, v[2:3]
	v_or_b32_e32 v10, 2, v14
	v_addc_co_u32_e32 v7, vcc, 0, v7, vcc
	v_lshl_add_u64 v[8:9], v[8:9], 0, v[192:193]
	v_mad_i64_i32 v[10:11], s[2:3], v10, s14, v[4:5]
	v_add_co_u32_e32 v8, vcc, 0x2000, v8
	v_lshl_add_u64 v[10:11], v[10:11], 0, v[2:3]
	v_or_b32_e32 v12, 3, v14
	v_addc_co_u32_e32 v9, vcc, 0, v9, vcc
	v_lshl_add_u64 v[10:11], v[10:11], 0, v[192:193]
	v_mad_i64_i32 v[12:13], s[2:3], v12, s14, v[4:5]
	v_add_co_u32_e32 v10, vcc, 0x2000, v10
	v_lshl_add_u64 v[12:13], v[12:13], 0, v[2:3]
	s_nop 0
	v_addc_co_u32_e32 v11, vcc, 0, v11, vcc
	v_lshl_add_u64 v[12:13], v[12:13], 0, v[192:193]
	v_add_co_u32_e32 v12, vcc, 0x2000, v12
	v_mov_b32_e32 v209, v234
	s_nop 0
	v_addc_co_u32_e32 v13, vcc, 0, v13, vcc
	global_load_dwordx2 v[168:169], v[6:7], off
	global_load_dwordx2 v[170:171], v[8:9], off
	global_load_dwordx2 v[172:173], v[10:11], off
	global_load_dwordx2 v[174:175], v[12:13], off
	v_or_b32_e32 v6, 4, v14
	v_mad_i64_i32 v[6:7], s[2:3], v6, s14, v[4:5]
	v_lshl_add_u64 v[6:7], v[6:7], 0, v[2:3]
	v_or_b32_e32 v8, 5, v14
	v_lshl_add_u64 v[6:7], v[6:7], 0, v[192:193]
	v_mad_i64_i32 v[8:9], s[2:3], v8, s14, v[4:5]
	v_add_co_u32_e32 v6, vcc, 0x2000, v6
	v_lshl_add_u64 v[8:9], v[8:9], 0, v[2:3]
	v_or_b32_e32 v10, 6, v14
	v_addc_co_u32_e32 v7, vcc, 0, v7, vcc
	v_lshl_add_u64 v[8:9], v[8:9], 0, v[192:193]
	v_mad_i64_i32 v[10:11], s[2:3], v10, s14, v[4:5]
	v_add_co_u32_e32 v8, vcc, 0x2000, v8
	v_lshl_add_u64 v[10:11], v[10:11], 0, v[2:3]
	v_or_b32_e32 v12, 7, v14
	v_addc_co_u32_e32 v9, vcc, 0, v9, vcc
	v_lshl_add_u64 v[10:11], v[10:11], 0, v[192:193]
	v_mad_i64_i32 v[4:5], s[2:3], v12, s14, v[4:5]
	v_add_co_u32_e32 v10, vcc, 0x2000, v10
	v_lshl_add_u64 v[4:5], v[4:5], 0, v[2:3]
	s_nop 0
	v_addc_co_u32_e32 v11, vcc, 0, v11, vcc
	v_lshl_add_u64 v[4:5], v[4:5], 0, v[192:193]
	v_add_co_u32_e32 v4, vcc, 0x2000, v4
	v_mov_b32_e32 v207, v233
	s_nop 0
	v_addc_co_u32_e32 v5, vcc, 0, v5, vcc
	global_load_dwordx2 v[180:181], v[6:7], off
	global_load_dwordx2 v[182:183], v[8:9], off
	global_load_dwordx2 v[184:185], v[10:11], off
	global_load_dwordx2 v[188:189], v[4:5], off
	s_branch .LBB0_4543
